# back-edge rotation (7.11) in the five GEMM main loops: counter/pointer updates and exit test moved in front of the iteration's last barrier (on top of v66)
# baseline (speedup 1.0000x reference)
.LBB0_247:
	ds_read_b128 v[130:133], v149
	ds_read_b128 v[134:137], v149 offset:1024
	ds_read_b128 v[168:171], v149 offset:2048
	ds_read_b128 v[172:175], v149 offset:3072
	ds_read_b128 v[176:179], v196
	ds_read_b128 v[180:183], v196 offset:1024
	ds_read_b128 v[184:187], v196 offset:2048
	ds_read_b128 v[188:191], v196 offset:3072
	s_add_u32 s14, s12, 0xfffc0080
	s_addc_u32 s15, s13, -1
	s_cmp_eq_u32 s48, 12
	s_cselect_b32 s53, s1, s15
	s_cselect_b32 s52, s2, s14
	s_cselect_b32 s15, s11, s43
	s_cselect_b32 s14, s33, s41
	v_lshl_add_u64 v[192:193], s[12:13], 0, v[160:161]
	s_add_i32 m0, s56, 0xc000
	ds_read_b128 v[204:207], v197
	ds_read_b128 v[208:211], v197 offset:1024
	ds_read_b128 v[212:215], v197 offset:2048
	ds_read_b128 v[216:219], v197 offset:3072
	ds_read_b128 v[220:223], v197 offset:4096
	ds_read_b128 v[224:227], v197 offset:5120
	ds_read_b128 v[228:231], v197 offset:6144
	ds_read_b128 v[232:235], v197 offset:7168
	global_load_lds_dwordx4 v[192:193], off
	v_lshl_add_u64 v[192:193], s[12:13], 0, v[162:163]
	s_add_i32 m0, s56, 0xe000
	s_nop 0
	global_load_lds_dwordx4 v[192:193], off
	s_waitcnt vmcnt(8)
	s_waitcnt lgkmcnt(0)
	s_barrier
	s_setprio 1
	s_waitcnt lgkmcnt(0)
	v_mfma_f32_16x16x32_bf16 v[126:129], v[130:133], v[204:207], v[126:129]
	v_mfma_f32_16x16x32_bf16 v[122:125], v[168:171], v[204:207], v[122:125]
	v_mfma_f32_16x16x32_bf16 v[110:113], v[130:133], v[212:215], v[110:113]
	v_mfma_f32_16x16x32_bf16 v[106:109], v[168:171], v[212:215], v[106:109]
	v_mfma_f32_16x16x32_bf16 v[94:97], v[130:133], v[220:223], v[94:97]
	v_mfma_f32_16x16x32_bf16 v[90:93], v[168:171], v[220:223], v[90:93]
	v_mfma_f32_16x16x32_bf16 v[78:81], v[130:133], v[228:231], v[78:81]
	v_mfma_f32_16x16x32_bf16 v[74:77], v[168:171], v[228:231], v[74:77]
	v_mfma_f32_16x16x32_bf16 v[126:129], v[134:137], v[208:211], v[126:129]
	v_mfma_f32_16x16x32_bf16 v[122:125], v[172:175], v[208:211], v[122:125]
	v_mfma_f32_16x16x32_bf16 v[110:113], v[134:137], v[216:219], v[110:113]
	v_mfma_f32_16x16x32_bf16 v[106:109], v[172:175], v[216:219], v[106:109]
	v_mfma_f32_16x16x32_bf16 v[94:97], v[134:137], v[224:227], v[94:97]
	v_mfma_f32_16x16x32_bf16 v[90:93], v[172:175], v[224:227], v[90:93]
	v_mfma_f32_16x16x32_bf16 v[78:81], v[134:137], v[232:235], v[78:81]
	v_mfma_f32_16x16x32_bf16 v[74:77], v[172:175], v[232:235], v[74:77]
	s_setprio 0
	s_setprio 1
	v_mfma_f32_16x16x32_bf16 v[118:121], v[176:179], v[204:207], v[118:121]
	v_mfma_f32_16x16x32_bf16 v[114:117], v[184:187], v[204:207], v[114:117]
	v_mfma_f32_16x16x32_bf16 v[102:105], v[176:179], v[212:215], v[102:105]
	v_mfma_f32_16x16x32_bf16 v[98:101], v[184:187], v[212:215], v[98:101]
	v_mfma_f32_16x16x32_bf16 v[86:89], v[176:179], v[220:223], v[86:89]
	v_mfma_f32_16x16x32_bf16 v[82:85], v[184:187], v[220:223], v[82:85]
	v_mfma_f32_16x16x32_bf16 v[70:73], v[176:179], v[228:231], v[70:73]
	v_mfma_f32_16x16x32_bf16 v[66:69], v[184:187], v[228:231], v[66:69]
	v_mfma_f32_16x16x32_bf16 v[118:121], v[180:183], v[208:211], v[118:121]
	v_mfma_f32_16x16x32_bf16 v[114:117], v[188:191], v[208:211], v[114:117]
	v_mfma_f32_16x16x32_bf16 v[102:105], v[180:183], v[216:219], v[102:105]
	v_mfma_f32_16x16x32_bf16 v[98:101], v[188:191], v[216:219], v[98:101]
	v_mfma_f32_16x16x32_bf16 v[86:89], v[180:183], v[224:227], v[86:89]
	v_mfma_f32_16x16x32_bf16 v[82:85], v[188:191], v[224:227], v[82:85]
	v_mfma_f32_16x16x32_bf16 v[70:73], v[180:183], v[232:235], v[70:73]
	v_mfma_f32_16x16x32_bf16 v[66:69], v[188:191], v[232:235], v[66:69]
	s_setprio 0
	s_barrier
	s_add_i32 s49, s67, s45
	v_lshl_add_u64 v[192:193], s[14:15], 0, v[140:141]
	s_mov_b32 m0, s49
	ds_read_b128 v[204:207], v197 offset:16384
	ds_read_b128 v[208:211], v197 offset:17408
	ds_read_b128 v[212:215], v197 offset:18432
	ds_read_b128 v[216:219], v197 offset:19456
	ds_read_b128 v[220:223], v197 offset:20480
	ds_read_b128 v[224:227], v197 offset:21504
	ds_read_b128 v[228:231], v197 offset:22528
	ds_read_b128 v[232:235], v197 offset:23552
	global_load_lds_dwordx4 v[192:193], off
	s_add_i32 m0, s49, 0x2000
	s_add_u32 s74, s14, 0x40000
	v_lshl_add_u64 v[236:237], s[14:15], 0, v[144:145]
	s_addc_u32 s75, s15, 0
	s_add_i32 s49, s68, s45
	global_load_lds_dwordx4 v[236:237], off
	v_lshl_add_u64 v[238:239], s[74:75], 0, v[140:141]
	s_mov_b32 m0, s49
	v_lshl_add_u64 v[240:241], s[52:53], 0, v[142:143]
	global_load_lds_dwordx4 v[238:239], off
	v_lshl_add_u64 v[238:239], s[74:75], 0, v[144:145]
	s_add_i32 m0, s49, 0x2000
	s_nop 0
	global_load_lds_dwordx4 v[238:239], off
	v_lshl_add_u64 v[238:239], s[52:53], 0, v[138:139]
	s_mov_b32 m0, s56
	s_nop 0
	global_load_lds_dwordx4 v[238:239], off
	s_mov_b32 m0, s57
	s_nop 0
	global_load_lds_dwordx4 v[240:241], off
	s_waitcnt vmcnt(8)
	s_waitcnt lgkmcnt(0)
	s_barrier
	s_setprio 1
	s_waitcnt lgkmcnt(0)
	v_mfma_f32_16x16x32_bf16 v[62:65], v[130:133], v[204:207], v[62:65]
	v_mfma_f32_16x16x32_bf16 v[58:61], v[168:171], v[204:207], v[58:61]
	v_mfma_f32_16x16x32_bf16 v[46:49], v[130:133], v[212:215], v[46:49]
	v_mfma_f32_16x16x32_bf16 v[42:45], v[168:171], v[212:215], v[42:45]
	v_mfma_f32_16x16x32_bf16 v[30:33], v[130:133], v[220:223], v[30:33]
	v_mfma_f32_16x16x32_bf16 v[26:29], v[168:171], v[220:223], v[26:29]
	v_mfma_f32_16x16x32_bf16 v[14:17], v[130:133], v[228:231], v[14:17]
	v_mfma_f32_16x16x32_bf16 v[10:13], v[168:171], v[228:231], v[10:13]
	v_mfma_f32_16x16x32_bf16 v[62:65], v[134:137], v[208:211], v[62:65]
	v_mfma_f32_16x16x32_bf16 v[58:61], v[172:175], v[208:211], v[58:61]
	v_mfma_f32_16x16x32_bf16 v[46:49], v[134:137], v[216:219], v[46:49]
	v_mfma_f32_16x16x32_bf16 v[42:45], v[172:175], v[216:219], v[42:45]
	v_mfma_f32_16x16x32_bf16 v[30:33], v[134:137], v[224:227], v[30:33]
	v_mfma_f32_16x16x32_bf16 v[26:29], v[172:175], v[224:227], v[26:29]
	v_mfma_f32_16x16x32_bf16 v[14:17], v[134:137], v[232:235], v[14:17]
	v_mfma_f32_16x16x32_bf16 v[10:13], v[172:175], v[232:235], v[10:13]
	s_setprio 0
	s_setprio 1
	v_mfma_f32_16x16x32_bf16 v[54:57], v[176:179], v[204:207], v[54:57]
	v_mfma_f32_16x16x32_bf16 v[50:53], v[184:187], v[204:207], v[50:53]
	v_mfma_f32_16x16x32_bf16 v[38:41], v[176:179], v[212:215], v[38:41]
	v_mfma_f32_16x16x32_bf16 v[34:37], v[184:187], v[212:215], v[34:37]
	v_mfma_f32_16x16x32_bf16 v[22:25], v[176:179], v[220:223], v[22:25]
	v_mfma_f32_16x16x32_bf16 v[18:21], v[184:187], v[220:223], v[18:21]
	v_mfma_f32_16x16x32_bf16 v[6:9], v[176:179], v[228:231], v[6:9]
	v_mfma_f32_16x16x32_bf16 v[2:5], v[184:187], v[228:231], v[2:5]
	v_mfma_f32_16x16x32_bf16 v[54:57], v[180:183], v[208:211], v[54:57]
	v_mfma_f32_16x16x32_bf16 v[50:53], v[188:191], v[208:211], v[50:53]
	v_mfma_f32_16x16x32_bf16 v[38:41], v[180:183], v[216:219], v[38:41]
	v_mfma_f32_16x16x32_bf16 v[34:37], v[188:191], v[216:219], v[34:37]
	v_mfma_f32_16x16x32_bf16 v[22:25], v[180:183], v[224:227], v[22:25]
	v_mfma_f32_16x16x32_bf16 v[18:21], v[188:191], v[224:227], v[18:21]
	v_mfma_f32_16x16x32_bf16 v[6:9], v[180:183], v[232:235], v[6:9]
	v_mfma_f32_16x16x32_bf16 v[2:5], v[188:191], v[232:235], v[2:5]
	s_setprio 0
	s_barrier
	s_add_i32 s49, 0, 0x18000
	v_add_u32_e32 v146, s49, v194
	s_add_i32 s73, 0, 0x1c000
	ds_read_b128 v[130:133], v146
	ds_read_b128 v[134:137], v146 offset:1024
	ds_read_b128 v[168:171], v146 offset:2048
	ds_read_b128 v[172:175], v146 offset:3072
	v_add_u32_e32 v146, s73, v194
	ds_read_b128 v[176:179], v146
	ds_read_b128 v[180:183], v146 offset:1024
	ds_read_b128 v[184:187], v146 offset:2048
	ds_read_b128 v[188:191], v146 offset:3072
	s_add_u32 s52, s52, 0x40000
	s_addc_u32 s53, s53, 0
	s_mov_b32 m0, s58
	v_lshl_add_u64 v[242:243], s[52:53], 0, v[138:139]
	ds_read_b128 v[204:207], v197 offset:32768
	ds_read_b128 v[208:211], v197 offset:33792
	ds_read_b128 v[212:215], v197 offset:34816
	ds_read_b128 v[216:219], v197 offset:35840
	ds_read_b128 v[220:223], v197 offset:36864
	ds_read_b128 v[224:227], v197 offset:37888
	ds_read_b128 v[228:231], v197 offset:38912
	ds_read_b128 v[232:235], v197 offset:39936
	global_load_lds_dwordx4 v[242:243], off
	v_lshl_add_u64 v[242:243], s[52:53], 0, v[142:143]
	s_mov_b32 m0, s59
	s_nop 0
	global_load_lds_dwordx4 v[242:243], off
	s_waitcnt vmcnt(8)
	s_waitcnt lgkmcnt(0)
	s_barrier
	s_setprio 1
	s_waitcnt lgkmcnt(0)
	v_mfma_f32_16x16x32_bf16 v[126:129], v[130:133], v[204:207], v[126:129]
	v_mfma_f32_16x16x32_bf16 v[122:125], v[168:171], v[204:207], v[122:125]
	v_mfma_f32_16x16x32_bf16 v[110:113], v[130:133], v[212:215], v[110:113]
	v_mfma_f32_16x16x32_bf16 v[106:109], v[168:171], v[212:215], v[106:109]
	v_mfma_f32_16x16x32_bf16 v[94:97], v[130:133], v[220:223], v[94:97]
	v_mfma_f32_16x16x32_bf16 v[90:93], v[168:171], v[220:223], v[90:93]
	v_mfma_f32_16x16x32_bf16 v[78:81], v[130:133], v[228:231], v[78:81]
	v_mfma_f32_16x16x32_bf16 v[74:77], v[168:171], v[228:231], v[74:77]
	v_mfma_f32_16x16x32_bf16 v[126:129], v[134:137], v[208:211], v[126:129]
	v_mfma_f32_16x16x32_bf16 v[122:125], v[172:175], v[208:211], v[122:125]
	v_mfma_f32_16x16x32_bf16 v[110:113], v[134:137], v[216:219], v[110:113]
	v_mfma_f32_16x16x32_bf16 v[106:109], v[172:175], v[216:219], v[106:109]
	v_mfma_f32_16x16x32_bf16 v[94:97], v[134:137], v[224:227], v[94:97]
	v_mfma_f32_16x16x32_bf16 v[90:93], v[172:175], v[224:227], v[90:93]
	v_mfma_f32_16x16x32_bf16 v[78:81], v[134:137], v[232:235], v[78:81]
	v_mfma_f32_16x16x32_bf16 v[74:77], v[172:175], v[232:235], v[74:77]
	s_setprio 0
	s_setprio 1
	v_mfma_f32_16x16x32_bf16 v[118:121], v[176:179], v[204:207], v[118:121]
	v_mfma_f32_16x16x32_bf16 v[114:117], v[184:187], v[204:207], v[114:117]
	v_mfma_f32_16x16x32_bf16 v[102:105], v[176:179], v[212:215], v[102:105]
	v_mfma_f32_16x16x32_bf16 v[98:101], v[184:187], v[212:215], v[98:101]
	v_mfma_f32_16x16x32_bf16 v[86:89], v[176:179], v[220:223], v[86:89]
	v_mfma_f32_16x16x32_bf16 v[82:85], v[184:187], v[220:223], v[82:85]
	v_mfma_f32_16x16x32_bf16 v[70:73], v[176:179], v[228:231], v[70:73]
	v_mfma_f32_16x16x32_bf16 v[66:69], v[184:187], v[228:231], v[66:69]
	v_mfma_f32_16x16x32_bf16 v[118:121], v[180:183], v[208:211], v[118:121]
	v_mfma_f32_16x16x32_bf16 v[114:117], v[188:191], v[208:211], v[114:117]
	v_mfma_f32_16x16x32_bf16 v[102:105], v[180:183], v[216:219], v[102:105]
	v_mfma_f32_16x16x32_bf16 v[98:101], v[188:191], v[216:219], v[98:101]
	v_mfma_f32_16x16x32_bf16 v[86:89], v[180:183], v[224:227], v[86:89]
	v_mfma_f32_16x16x32_bf16 v[82:85], v[188:191], v[224:227], v[82:85]
	v_mfma_f32_16x16x32_bf16 v[70:73], v[180:183], v[232:235], v[70:73]
	v_mfma_f32_16x16x32_bf16 v[66:69], v[188:191], v[232:235], v[66:69]
	s_setprio 0
	s_barrier
	s_add_i32 s49, s49, s45
	v_lshl_add_u64 v[192:193], v[192:193], 0, s[22:23]
	s_mov_b32 m0, s49
	ds_read_b128 v[204:207], v197 offset:49152
	ds_read_b128 v[208:211], v197 offset:50176
	ds_read_b128 v[212:215], v197 offset:51200
	ds_read_b128 v[216:219], v197 offset:52224
	ds_read_b128 v[220:223], v197 offset:53248
	ds_read_b128 v[224:227], v197 offset:54272
	ds_read_b128 v[228:231], v197 offset:55296
	ds_read_b128 v[232:235], v197 offset:56320
	global_load_lds_dwordx4 v[192:193], off
	s_add_i32 m0, s49, 0x2000
	s_add_u32 s14, s14, 0x40080
	v_lshl_add_u64 v[192:193], v[236:237], 0, s[22:23]
	s_addc_u32 s15, s15, 0
	s_add_i32 s49, s73, s45
	global_load_lds_dwordx4 v[192:193], off
	v_lshl_add_u64 v[192:193], s[14:15], 0, v[140:141]
	s_mov_b32 m0, s49
	s_nop 0
	global_load_lds_dwordx4 v[192:193], off
	v_lshl_add_u64 v[192:193], s[14:15], 0, v[144:145]
	s_add_i32 m0, s49, 0x2000
	s_nop 0
	global_load_lds_dwordx4 v[192:193], off
	v_lshl_add_u64 v[192:193], v[238:239], 0, s[22:23]
	s_mov_b32 m0, s63
	s_nop 0
	global_load_lds_dwordx4 v[192:193], off
	v_lshl_add_u64 v[192:193], v[240:241], 0, s[22:23]
	s_mov_b32 m0, s64
	s_nop 0
	global_load_lds_dwordx4 v[192:193], off
	s_waitcnt vmcnt(8)
	s_waitcnt lgkmcnt(0)
	s_barrier
	s_setprio 1
	s_waitcnt lgkmcnt(0)
	v_mfma_f32_16x16x32_bf16 v[62:65], v[130:133], v[204:207], v[62:65]
	v_mfma_f32_16x16x32_bf16 v[58:61], v[168:171], v[204:207], v[58:61]
	v_mfma_f32_16x16x32_bf16 v[46:49], v[130:133], v[212:215], v[46:49]
	v_mfma_f32_16x16x32_bf16 v[42:45], v[168:171], v[212:215], v[42:45]
	v_mfma_f32_16x16x32_bf16 v[30:33], v[130:133], v[220:223], v[30:33]
	v_mfma_f32_16x16x32_bf16 v[26:29], v[168:171], v[220:223], v[26:29]
	v_mfma_f32_16x16x32_bf16 v[14:17], v[130:133], v[228:231], v[14:17]
	v_mfma_f32_16x16x32_bf16 v[10:13], v[168:171], v[228:231], v[10:13]
	v_mfma_f32_16x16x32_bf16 v[62:65], v[134:137], v[208:211], v[62:65]
	v_mfma_f32_16x16x32_bf16 v[58:61], v[172:175], v[208:211], v[58:61]
	v_mfma_f32_16x16x32_bf16 v[46:49], v[134:137], v[216:219], v[46:49]
	v_mfma_f32_16x16x32_bf16 v[42:45], v[172:175], v[216:219], v[42:45]
	v_mfma_f32_16x16x32_bf16 v[30:33], v[134:137], v[224:227], v[30:33]
	v_mfma_f32_16x16x32_bf16 v[26:29], v[172:175], v[224:227], v[26:29]
	v_mfma_f32_16x16x32_bf16 v[14:17], v[134:137], v[232:235], v[14:17]
	v_mfma_f32_16x16x32_bf16 v[10:13], v[172:175], v[232:235], v[10:13]
	s_setprio 0
	s_setprio 1
	v_mfma_f32_16x16x32_bf16 v[54:57], v[176:179], v[204:207], v[54:57]
	v_mfma_f32_16x16x32_bf16 v[50:53], v[184:187], v[204:207], v[50:53]
	v_mfma_f32_16x16x32_bf16 v[38:41], v[176:179], v[212:215], v[38:41]
	v_mfma_f32_16x16x32_bf16 v[34:37], v[184:187], v[212:215], v[34:37]
	v_mfma_f32_16x16x32_bf16 v[22:25], v[176:179], v[220:223], v[22:25]
	v_mfma_f32_16x16x32_bf16 v[18:21], v[184:187], v[220:223], v[18:21]
	v_mfma_f32_16x16x32_bf16 v[6:9], v[176:179], v[228:231], v[6:9]
	v_mfma_f32_16x16x32_bf16 v[2:5], v[184:187], v[228:231], v[2:5]
	v_mfma_f32_16x16x32_bf16 v[54:57], v[180:183], v[208:211], v[54:57]
	v_mfma_f32_16x16x32_bf16 v[50:53], v[188:191], v[208:211], v[50:53]
	v_mfma_f32_16x16x32_bf16 v[38:41], v[180:183], v[216:219], v[38:41]
	v_mfma_f32_16x16x32_bf16 v[34:37], v[188:191], v[216:219], v[34:37]
	v_mfma_f32_16x16x32_bf16 v[22:25], v[180:183], v[224:227], v[22:25]
	v_mfma_f32_16x16x32_bf16 v[18:21], v[188:191], v[224:227], v[18:21]
	v_mfma_f32_16x16x32_bf16 v[6:9], v[180:183], v[232:235], v[6:9]
	v_mfma_f32_16x16x32_bf16 v[2:5], v[188:191], v[232:235], v[2:5]
	s_setprio 0
	s_add_i32 s48, s48, 2
	s_add_u32 s12, s12, 0x100
	s_addc_u32 s13, s13, 0
	s_add_u32 s41, s41, 0x100
	s_addc_u32 s43, s43, 0
	s_cmp_gt_u32 s48, 13
	s_barrier
	s_cbranch_scc0 .LBB0_247
	s_and_b64 vcc, exec, s[24:25]
	s_cbranch_vccz .LBB0_250
	s_barrier

.LBB0_1493:
	v_add_u32_e32 v3, s51, v156
	ds_read_b128 v[150:153], v3
	ds_read_b128 v[160:163], v3 offset:1024
	ds_read_b128 v[164:167], v3 offset:2048
	ds_read_b128 v[168:171], v3 offset:3072
	v_add_u32_e32 v3, s52, v156
	ds_read_b128 v[172:175], v3
	ds_read_b128 v[176:179], v3 offset:1024
	ds_read_b128 v[180:183], v3 offset:2048
	ds_read_b128 v[184:187], v3 offset:3072
	s_add_u32 s38, s36, 0xfffe0080
	s_addc_u32 s39, s37, -1
	s_cmp_eq_u32 s55, 4
	s_cselect_b32 s41, s7, s39
	s_cselect_b32 s40, s27, s38
	s_cselect_b32 s39, s25, s54
	s_cselect_b32 s38, s35, s53
	v_lshl_add_u64 v[4:5], s[36:37], 0, v[142:143]
	s_add_i32 m0, s43, 0xc000
	ds_read_b128 v[188:191], v158
	ds_read_b128 v[192:195], v158 offset:1024
	ds_read_b128 v[196:199], v158 offset:2048
	ds_read_b128 v[202:205], v158 offset:3072
	ds_read_b128 v[206:209], v158 offset:4096
	ds_read_b128 v[210:213], v158 offset:5120
	ds_read_b128 v[214:217], v158 offset:6144
	ds_read_b128 v[218:221], v158 offset:7168
	global_load_lds_dwordx4 v[4:5], off
	v_lshl_add_u64 v[4:5], s[36:37], 0, v[144:145]
	s_add_i32 m0, s43, 0xe000
	s_nop 0
	global_load_lds_dwordx4 v[4:5], off
	s_waitcnt vmcnt(8)
	s_waitcnt lgkmcnt(0)
	s_barrier
	s_setprio 1
	s_waitcnt lgkmcnt(0)
	v_mfma_f32_16x16x32_bf16 v[130:133], v[150:153], v[188:191], v[130:133]
	v_mfma_f32_16x16x32_bf16 v[126:129], v[164:167], v[188:191], v[126:129]
	v_mfma_f32_16x16x32_bf16 v[122:125], v[150:153], v[196:199], v[122:125]
	v_mfma_f32_16x16x32_bf16 v[118:121], v[164:167], v[196:199], v[118:121]
	v_mfma_f32_16x16x32_bf16 v[114:117], v[150:153], v[206:209], v[114:117]
	v_mfma_f32_16x16x32_bf16 v[110:113], v[164:167], v[206:209], v[110:113]
	v_mfma_f32_16x16x32_bf16 v[106:109], v[150:153], v[214:217], v[106:109]
	v_mfma_f32_16x16x32_bf16 v[102:105], v[164:167], v[214:217], v[102:105]
	v_mfma_f32_16x16x32_bf16 v[130:133], v[160:163], v[192:195], v[130:133]
	v_mfma_f32_16x16x32_bf16 v[126:129], v[168:171], v[192:195], v[126:129]
	v_mfma_f32_16x16x32_bf16 v[122:125], v[160:163], v[202:205], v[122:125]
	v_mfma_f32_16x16x32_bf16 v[118:121], v[168:171], v[202:205], v[118:121]
	v_mfma_f32_16x16x32_bf16 v[114:117], v[160:163], v[210:213], v[114:117]
	v_mfma_f32_16x16x32_bf16 v[110:113], v[168:171], v[210:213], v[110:113]
	v_mfma_f32_16x16x32_bf16 v[106:109], v[160:163], v[218:221], v[106:109]
	v_mfma_f32_16x16x32_bf16 v[102:105], v[168:171], v[218:221], v[102:105]
	s_setprio 0
	s_setprio 1
	v_mfma_f32_16x16x32_bf16 v[98:101], v[172:175], v[188:191], v[98:101]
	v_mfma_f32_16x16x32_bf16 v[94:97], v[180:183], v[188:191], v[94:97]
	v_mfma_f32_16x16x32_bf16 v[90:93], v[172:175], v[196:199], v[90:93]
	v_mfma_f32_16x16x32_bf16 v[86:89], v[180:183], v[196:199], v[86:89]
	v_mfma_f32_16x16x32_bf16 v[82:85], v[172:175], v[206:209], v[82:85]
	v_mfma_f32_16x16x32_bf16 v[78:81], v[180:183], v[206:209], v[78:81]
	v_mfma_f32_16x16x32_bf16 v[74:77], v[172:175], v[214:217], v[74:77]
	v_mfma_f32_16x16x32_bf16 v[70:73], v[180:183], v[214:217], v[70:73]
	v_mfma_f32_16x16x32_bf16 v[98:101], v[176:179], v[192:195], v[98:101]
	v_mfma_f32_16x16x32_bf16 v[94:97], v[184:187], v[192:195], v[94:97]
	v_mfma_f32_16x16x32_bf16 v[90:93], v[176:179], v[202:205], v[90:93]
	v_mfma_f32_16x16x32_bf16 v[86:89], v[184:187], v[202:205], v[86:89]
	v_mfma_f32_16x16x32_bf16 v[82:85], v[176:179], v[210:213], v[82:85]
	v_mfma_f32_16x16x32_bf16 v[78:81], v[184:187], v[210:213], v[78:81]
	v_mfma_f32_16x16x32_bf16 v[74:77], v[176:179], v[218:221], v[74:77]
	v_mfma_f32_16x16x32_bf16 v[70:73], v[184:187], v[218:221], v[70:73]
	s_setprio 0
	s_barrier
	s_add_i32 s56, s51, s42
	v_lshl_add_u64 v[154:155], s[38:39], 0, v[136:137]
	s_mov_b32 m0, s56
	ds_read_b128 v[188:191], v158 offset:16384
	ds_read_b128 v[192:195], v158 offset:17408
	ds_read_b128 v[196:199], v158 offset:18432
	ds_read_b128 v[202:205], v158 offset:19456
	ds_read_b128 v[206:209], v158 offset:20480
	ds_read_b128 v[210:213], v158 offset:21504
	ds_read_b128 v[214:217], v158 offset:22528
	ds_read_b128 v[218:221], v158 offset:23552
	global_load_lds_dwordx4 v[154:155], off
	s_add_i32 m0, s56, 0x2000
	s_add_u32 s56, s38, 0x20000
	v_lshl_add_u64 v[222:223], s[38:39], 0, v[140:141]
	s_addc_u32 s57, s39, 0
	s_add_i32 s58, s52, s42
	global_load_lds_dwordx4 v[222:223], off
	v_lshl_add_u64 v[4:5], s[56:57], 0, v[136:137]
	s_mov_b32 m0, s58
	v_lshl_add_u64 v[224:225], s[40:41], 0, v[134:135]
	global_load_lds_dwordx4 v[4:5], off
	v_lshl_add_u64 v[4:5], s[56:57], 0, v[140:141]
	s_add_i32 m0, s58, 0x2000
	v_lshl_add_u64 v[226:227], s[40:41], 0, v[138:139]
	global_load_lds_dwordx4 v[4:5], off
	s_mov_b32 m0, s43
	s_nop 0
	global_load_lds_dwordx4 v[224:225], off
	s_mov_b32 m0, s44
	s_nop 0
	global_load_lds_dwordx4 v[226:227], off
	s_waitcnt vmcnt(8)
	s_waitcnt lgkmcnt(0)
	s_barrier
	s_setprio 1
	s_waitcnt lgkmcnt(0)
	v_mfma_f32_16x16x32_bf16 v[66:69], v[150:153], v[188:191], v[66:69]
	v_mfma_f32_16x16x32_bf16 v[62:65], v[164:167], v[188:191], v[62:65]
	v_mfma_f32_16x16x32_bf16 v[58:61], v[150:153], v[196:199], v[58:61]
	v_mfma_f32_16x16x32_bf16 v[54:57], v[164:167], v[196:199], v[54:57]
	v_mfma_f32_16x16x32_bf16 v[50:53], v[150:153], v[206:209], v[50:53]
	v_mfma_f32_16x16x32_bf16 v[46:49], v[164:167], v[206:209], v[46:49]
	v_mfma_f32_16x16x32_bf16 v[42:45], v[150:153], v[214:217], v[42:45]
	v_mfma_f32_16x16x32_bf16 v[38:41], v[164:167], v[214:217], v[38:41]
	v_mfma_f32_16x16x32_bf16 v[66:69], v[160:163], v[192:195], v[66:69]
	v_mfma_f32_16x16x32_bf16 v[62:65], v[168:171], v[192:195], v[62:65]
	v_mfma_f32_16x16x32_bf16 v[58:61], v[160:163], v[202:205], v[58:61]
	v_mfma_f32_16x16x32_bf16 v[54:57], v[168:171], v[202:205], v[54:57]
	v_mfma_f32_16x16x32_bf16 v[50:53], v[160:163], v[210:213], v[50:53]
	v_mfma_f32_16x16x32_bf16 v[46:49], v[168:171], v[210:213], v[46:49]
	v_mfma_f32_16x16x32_bf16 v[42:45], v[160:163], v[218:221], v[42:45]
	v_mfma_f32_16x16x32_bf16 v[38:41], v[168:171], v[218:221], v[38:41]
	s_setprio 0
	s_setprio 1
	v_mfma_f32_16x16x32_bf16 v[34:37], v[172:175], v[188:191], v[34:37]
	v_mfma_f32_16x16x32_bf16 v[30:33], v[180:183], v[188:191], v[30:33]
	v_mfma_f32_16x16x32_bf16 v[26:29], v[172:175], v[196:199], v[26:29]
	v_mfma_f32_16x16x32_bf16 v[22:25], v[180:183], v[196:199], v[22:25]
	v_mfma_f32_16x16x32_bf16 v[18:21], v[172:175], v[206:209], v[18:21]
	v_mfma_f32_16x16x32_bf16 v[14:17], v[180:183], v[206:209], v[14:17]
	v_mfma_f32_16x16x32_bf16 v[10:13], v[172:175], v[214:217], v[10:13]
	v_mfma_f32_16x16x32_bf16 v[4:7], v[180:183], v[214:217], v[6:9]
	v_mfma_f32_16x16x32_bf16 v[34:37], v[176:179], v[192:195], v[34:37]
	v_mfma_f32_16x16x32_bf16 v[30:33], v[184:187], v[192:195], v[30:33]
	v_mfma_f32_16x16x32_bf16 v[26:29], v[176:179], v[202:205], v[26:29]
	v_mfma_f32_16x16x32_bf16 v[22:25], v[184:187], v[202:205], v[22:25]
	v_mfma_f32_16x16x32_bf16 v[18:21], v[176:179], v[210:213], v[18:21]
	v_mfma_f32_16x16x32_bf16 v[14:17], v[184:187], v[210:213], v[14:17]
	v_mfma_f32_16x16x32_bf16 v[10:13], v[176:179], v[218:221], v[10:13]
	v_mfma_f32_16x16x32_bf16 v[4:7], v[184:187], v[218:221], v[4:7]
	s_setprio 0
	s_barrier
	s_add_i32 s56, 0, 0x18000
	v_add_u32_e32 v3, s56, v156
	s_add_i32 s57, 0, 0x1c000
	ds_read_b128 v[150:153], v3
	ds_read_b128 v[160:163], v3 offset:1024
	ds_read_b128 v[164:167], v3 offset:2048
	ds_read_b128 v[168:171], v3 offset:3072
	v_add_u32_e32 v3, s57, v156
	ds_read_b128 v[172:175], v3
	ds_read_b128 v[176:179], v3 offset:1024
	ds_read_b128 v[180:183], v3 offset:2048
	ds_read_b128 v[184:187], v3 offset:3072
	s_add_u32 s40, s40, 0x20000
	s_addc_u32 s41, s41, 0
	s_mov_b32 m0, s45
	v_lshl_add_u64 v[8:9], s[40:41], 0, v[134:135]
	ds_read_b128 v[188:191], v158 offset:32768
	ds_read_b128 v[192:195], v158 offset:33792
	ds_read_b128 v[196:199], v158 offset:34816
	ds_read_b128 v[202:205], v158 offset:35840
	ds_read_b128 v[206:209], v158 offset:36864
	ds_read_b128 v[210:213], v158 offset:37888
	ds_read_b128 v[214:217], v158 offset:38912
	ds_read_b128 v[218:221], v158 offset:39936
	global_load_lds_dwordx4 v[8:9], off
	v_lshl_add_u64 v[8:9], s[40:41], 0, v[138:139]
	s_mov_b32 m0, s46
	s_nop 0
	global_load_lds_dwordx4 v[8:9], off
	s_waitcnt vmcnt(8)
	s_waitcnt lgkmcnt(0)
	s_barrier
	s_setprio 1
	s_waitcnt lgkmcnt(0)
	v_mfma_f32_16x16x32_bf16 v[130:133], v[150:153], v[188:191], v[130:133]
	v_mfma_f32_16x16x32_bf16 v[126:129], v[164:167], v[188:191], v[126:129]
	v_mfma_f32_16x16x32_bf16 v[122:125], v[150:153], v[196:199], v[122:125]
	v_mfma_f32_16x16x32_bf16 v[118:121], v[164:167], v[196:199], v[118:121]
	v_mfma_f32_16x16x32_bf16 v[114:117], v[150:153], v[206:209], v[114:117]
	v_mfma_f32_16x16x32_bf16 v[110:113], v[164:167], v[206:209], v[110:113]
	v_mfma_f32_16x16x32_bf16 v[106:109], v[150:153], v[214:217], v[106:109]
	v_mfma_f32_16x16x32_bf16 v[102:105], v[164:167], v[214:217], v[102:105]
	v_mfma_f32_16x16x32_bf16 v[130:133], v[160:163], v[192:195], v[130:133]
	v_mfma_f32_16x16x32_bf16 v[126:129], v[168:171], v[192:195], v[126:129]
	v_mfma_f32_16x16x32_bf16 v[122:125], v[160:163], v[202:205], v[122:125]
	v_mfma_f32_16x16x32_bf16 v[118:121], v[168:171], v[202:205], v[118:121]
	v_mfma_f32_16x16x32_bf16 v[114:117], v[160:163], v[210:213], v[114:117]
	v_mfma_f32_16x16x32_bf16 v[110:113], v[168:171], v[210:213], v[110:113]
	v_mfma_f32_16x16x32_bf16 v[106:109], v[160:163], v[218:221], v[106:109]
	v_mfma_f32_16x16x32_bf16 v[102:105], v[168:171], v[218:221], v[102:105]
	s_setprio 0
	s_setprio 1
	v_mfma_f32_16x16x32_bf16 v[98:101], v[172:175], v[188:191], v[98:101]
	v_mfma_f32_16x16x32_bf16 v[94:97], v[180:183], v[188:191], v[94:97]
	v_mfma_f32_16x16x32_bf16 v[90:93], v[172:175], v[196:199], v[90:93]
	v_mfma_f32_16x16x32_bf16 v[86:89], v[180:183], v[196:199], v[86:89]
	v_mfma_f32_16x16x32_bf16 v[82:85], v[172:175], v[206:209], v[82:85]
	v_mfma_f32_16x16x32_bf16 v[78:81], v[180:183], v[206:209], v[78:81]
	v_mfma_f32_16x16x32_bf16 v[74:77], v[172:175], v[214:217], v[74:77]
	v_mfma_f32_16x16x32_bf16 v[70:73], v[180:183], v[214:217], v[70:73]
	v_mfma_f32_16x16x32_bf16 v[98:101], v[176:179], v[192:195], v[98:101]
	v_mfma_f32_16x16x32_bf16 v[94:97], v[184:187], v[192:195], v[94:97]
	v_mfma_f32_16x16x32_bf16 v[90:93], v[176:179], v[202:205], v[90:93]
	v_mfma_f32_16x16x32_bf16 v[86:89], v[184:187], v[202:205], v[86:89]
	v_mfma_f32_16x16x32_bf16 v[82:85], v[176:179], v[210:213], v[82:85]
	v_mfma_f32_16x16x32_bf16 v[78:81], v[184:187], v[210:213], v[78:81]
	v_mfma_f32_16x16x32_bf16 v[74:77], v[176:179], v[218:221], v[74:77]
	v_mfma_f32_16x16x32_bf16 v[70:73], v[184:187], v[218:221], v[70:73]
	s_setprio 0
	s_barrier
	s_add_i32 s40, s56, s42
	v_lshl_add_u64 v[8:9], v[154:155], 0, s[10:11]
	s_mov_b32 m0, s40
	ds_read_b128 v[188:191], v158 offset:49152
	ds_read_b128 v[192:195], v158 offset:50176
	ds_read_b128 v[196:199], v158 offset:51200
	ds_read_b128 v[202:205], v158 offset:52224
	ds_read_b128 v[206:209], v158 offset:53248
	ds_read_b128 v[210:213], v158 offset:54272
	ds_read_b128 v[214:217], v158 offset:55296
	ds_read_b128 v[218:221], v158 offset:56320
	global_load_lds_dwordx4 v[8:9], off
	s_add_i32 m0, s40, 0x2000
	s_add_u32 s38, s38, 0x20080
	v_lshl_add_u64 v[8:9], v[222:223], 0, s[10:11]
	s_addc_u32 s39, s39, 0
	s_add_i32 s40, s57, s42
	global_load_lds_dwordx4 v[8:9], off
	v_lshl_add_u64 v[8:9], s[38:39], 0, v[136:137]
	s_mov_b32 m0, s40
	s_nop 0
	global_load_lds_dwordx4 v[8:9], off
	v_lshl_add_u64 v[8:9], s[38:39], 0, v[140:141]
	s_add_i32 m0, s40, 0x2000
	s_nop 0
	global_load_lds_dwordx4 v[8:9], off
	v_lshl_add_u64 v[8:9], v[224:225], 0, s[10:11]
	s_mov_b32 m0, s47
	s_nop 0
	global_load_lds_dwordx4 v[8:9], off
	v_lshl_add_u64 v[8:9], v[226:227], 0, s[10:11]
	s_mov_b32 m0, s48
	s_nop 0
	global_load_lds_dwordx4 v[8:9], off
	s_waitcnt vmcnt(8)
	s_waitcnt lgkmcnt(0)
	s_barrier
	s_setprio 1
	s_waitcnt lgkmcnt(0)
	v_mfma_f32_16x16x32_bf16 v[66:69], v[150:153], v[188:191], v[66:69]
	v_mfma_f32_16x16x32_bf16 v[62:65], v[164:167], v[188:191], v[62:65]
	v_mfma_f32_16x16x32_bf16 v[58:61], v[150:153], v[196:199], v[58:61]
	v_mfma_f32_16x16x32_bf16 v[54:57], v[164:167], v[196:199], v[54:57]
	v_mfma_f32_16x16x32_bf16 v[50:53], v[150:153], v[206:209], v[50:53]
	v_mfma_f32_16x16x32_bf16 v[46:49], v[164:167], v[206:209], v[46:49]
	v_mfma_f32_16x16x32_bf16 v[42:45], v[150:153], v[214:217], v[42:45]
	v_mfma_f32_16x16x32_bf16 v[38:41], v[164:167], v[214:217], v[38:41]
	v_mfma_f32_16x16x32_bf16 v[66:69], v[160:163], v[192:195], v[66:69]
	v_mfma_f32_16x16x32_bf16 v[62:65], v[168:171], v[192:195], v[62:65]
	v_mfma_f32_16x16x32_bf16 v[58:61], v[160:163], v[202:205], v[58:61]
	v_mfma_f32_16x16x32_bf16 v[54:57], v[168:171], v[202:205], v[54:57]
	v_mfma_f32_16x16x32_bf16 v[50:53], v[160:163], v[210:213], v[50:53]
	v_mfma_f32_16x16x32_bf16 v[46:49], v[168:171], v[210:213], v[46:49]
	v_mfma_f32_16x16x32_bf16 v[42:45], v[160:163], v[218:221], v[42:45]
	v_mfma_f32_16x16x32_bf16 v[38:41], v[168:171], v[218:221], v[38:41]
	s_setprio 0
	s_setprio 1
	v_mfma_f32_16x16x32_bf16 v[34:37], v[172:175], v[188:191], v[34:37]
	v_mfma_f32_16x16x32_bf16 v[30:33], v[180:183], v[188:191], v[30:33]
	v_mfma_f32_16x16x32_bf16 v[26:29], v[172:175], v[196:199], v[26:29]
	v_mfma_f32_16x16x32_bf16 v[22:25], v[180:183], v[196:199], v[22:25]
	v_mfma_f32_16x16x32_bf16 v[18:21], v[172:175], v[206:209], v[18:21]
	v_mfma_f32_16x16x32_bf16 v[14:17], v[180:183], v[206:209], v[14:17]
	v_mfma_f32_16x16x32_bf16 v[8:11], v[172:175], v[214:217], v[10:13]
	v_mfma_f32_16x16x32_bf16 v[4:7], v[180:183], v[214:217], v[4:7]
	v_mfma_f32_16x16x32_bf16 v[34:37], v[176:179], v[192:195], v[34:37]
	v_mfma_f32_16x16x32_bf16 v[30:33], v[184:187], v[192:195], v[30:33]
	v_mfma_f32_16x16x32_bf16 v[26:29], v[176:179], v[202:205], v[26:29]
	v_mfma_f32_16x16x32_bf16 v[22:25], v[184:187], v[202:205], v[22:25]
	v_mfma_f32_16x16x32_bf16 v[18:21], v[176:179], v[210:213], v[18:21]
	v_mfma_f32_16x16x32_bf16 v[14:17], v[184:187], v[210:213], v[14:17]
	v_mfma_f32_16x16x32_bf16 v[10:13], v[176:179], v[218:221], v[8:11]
	v_mfma_f32_16x16x32_bf16 v[6:9], v[184:187], v[218:221], v[4:7]
	s_setprio 0
	s_add_i32 s55, s55, 2
	s_add_u32 s36, s36, 0x100
	s_addc_u32 s37, s37, 0
	s_add_u32 s53, s53, 0x100
	s_addc_u32 s54, s54, 0
	s_cmp_gt_u32 s55, 5
	s_barrier
	s_cbranch_scc0 .LBB0_1493
	s_and_b64 vcc, exec, s[12:13]
	s_cbranch_vccz .LBB0_1496
	s_barrier

.LBB0_1640:
	ds_read_b128 v[146:149], v158
	ds_read_b128 v[150:153], v158 offset:1024
	ds_read_b128 v[162:165], v158 offset:2048
	ds_read_b128 v[166:169], v158 offset:3072
	ds_read_b128 v[170:173], v159
	ds_read_b128 v[174:177], v159 offset:1024
	ds_read_b128 v[178:181], v159 offset:2048
	ds_read_b128 v[182:185], v159 offset:3072
	s_add_u32 s34, s30, 0xfffc0080
	s_addc_u32 s35, s31, -1
	s_cmp_eq_u32 s57, 12
	s_cselect_b32 s37, s23, s35
	s_cselect_b32 s36, s29, s34
	s_cselect_b32 s35, s21, s56
	s_cselect_b32 s34, s54, s55
	v_lshl_add_u64 v[154:155], s[30:31], 0, v[138:139]
	s_add_i32 m0, s40, 0xc000
	ds_read_b128 v[186:189], v160
	ds_read_b128 v[190:193], v160 offset:1024
	ds_read_b128 v[194:197], v160 offset:2048
	ds_read_b128 v[202:205], v160 offset:3072
	ds_read_b128 v[206:209], v160 offset:4096
	ds_read_b128 v[210:213], v160 offset:5120
	ds_read_b128 v[214:217], v160 offset:6144
	ds_read_b128 v[218:221], v160 offset:7168
	global_load_lds_dwordx4 v[154:155], off
	v_lshl_add_u64 v[154:155], s[30:31], 0, v[140:141]
	s_add_i32 m0, s40, 0xe000
	s_nop 0
	global_load_lds_dwordx4 v[154:155], off
	s_waitcnt vmcnt(8)
	s_waitcnt lgkmcnt(0)
	s_barrier
	s_setprio 1
	s_waitcnt lgkmcnt(0)
	v_mfma_f32_16x16x32_bf16 v[126:129], v[146:149], v[186:189], v[126:129]
	v_mfma_f32_16x16x32_bf16 v[122:125], v[162:165], v[186:189], v[122:125]
	v_mfma_f32_16x16x32_bf16 v[110:113], v[146:149], v[194:197], v[110:113]
	v_mfma_f32_16x16x32_bf16 v[106:109], v[162:165], v[194:197], v[106:109]
	v_mfma_f32_16x16x32_bf16 v[94:97], v[146:149], v[206:209], v[94:97]
	v_mfma_f32_16x16x32_bf16 v[90:93], v[162:165], v[206:209], v[90:93]
	v_mfma_f32_16x16x32_bf16 v[78:81], v[146:149], v[214:217], v[78:81]
	v_mfma_f32_16x16x32_bf16 v[74:77], v[162:165], v[214:217], v[74:77]
	v_mfma_f32_16x16x32_bf16 v[126:129], v[150:153], v[190:193], v[126:129]
	v_mfma_f32_16x16x32_bf16 v[122:125], v[166:169], v[190:193], v[122:125]
	v_mfma_f32_16x16x32_bf16 v[110:113], v[150:153], v[202:205], v[110:113]
	v_mfma_f32_16x16x32_bf16 v[106:109], v[166:169], v[202:205], v[106:109]
	v_mfma_f32_16x16x32_bf16 v[94:97], v[150:153], v[210:213], v[94:97]
	v_mfma_f32_16x16x32_bf16 v[90:93], v[166:169], v[210:213], v[90:93]
	v_mfma_f32_16x16x32_bf16 v[78:81], v[150:153], v[218:221], v[78:81]
	v_mfma_f32_16x16x32_bf16 v[74:77], v[166:169], v[218:221], v[74:77]
	s_setprio 0
	s_setprio 1
	v_mfma_f32_16x16x32_bf16 v[118:121], v[170:173], v[186:189], v[118:121]
	v_mfma_f32_16x16x32_bf16 v[114:117], v[178:181], v[186:189], v[114:117]
	v_mfma_f32_16x16x32_bf16 v[102:105], v[170:173], v[194:197], v[102:105]
	v_mfma_f32_16x16x32_bf16 v[98:101], v[178:181], v[194:197], v[98:101]
	v_mfma_f32_16x16x32_bf16 v[86:89], v[170:173], v[206:209], v[86:89]
	v_mfma_f32_16x16x32_bf16 v[82:85], v[178:181], v[206:209], v[82:85]
	v_mfma_f32_16x16x32_bf16 v[70:73], v[170:173], v[214:217], v[70:73]
	v_mfma_f32_16x16x32_bf16 v[66:69], v[178:181], v[214:217], v[66:69]
	v_mfma_f32_16x16x32_bf16 v[118:121], v[174:177], v[190:193], v[118:121]
	v_mfma_f32_16x16x32_bf16 v[114:117], v[182:185], v[190:193], v[114:117]
	v_mfma_f32_16x16x32_bf16 v[102:105], v[174:177], v[202:205], v[102:105]
	v_mfma_f32_16x16x32_bf16 v[98:101], v[182:185], v[202:205], v[98:101]
	v_mfma_f32_16x16x32_bf16 v[86:89], v[174:177], v[210:213], v[86:89]
	v_mfma_f32_16x16x32_bf16 v[82:85], v[182:185], v[210:213], v[82:85]
	v_mfma_f32_16x16x32_bf16 v[70:73], v[174:177], v[218:221], v[70:73]
	v_mfma_f32_16x16x32_bf16 v[66:69], v[182:185], v[218:221], v[66:69]
	s_setprio 0
	s_barrier
	s_add_i32 s58, s51, s39
	v_lshl_add_u64 v[154:155], s[34:35], 0, v[132:133]
	s_mov_b32 m0, s58
	ds_read_b128 v[186:189], v160 offset:16384
	ds_read_b128 v[190:193], v160 offset:17408
	ds_read_b128 v[194:197], v160 offset:18432
	ds_read_b128 v[202:205], v160 offset:19456
	ds_read_b128 v[206:209], v160 offset:20480
	ds_read_b128 v[210:213], v160 offset:21504
	ds_read_b128 v[214:217], v160 offset:22528
	ds_read_b128 v[218:221], v160 offset:23552
	global_load_lds_dwordx4 v[154:155], off
	s_add_i32 m0, s58, 0x2000
	s_add_u32 s58, s34, 0x40000
	v_lshl_add_u64 v[198:199], s[34:35], 0, v[136:137]
	s_addc_u32 s59, s35, 0
	s_add_i32 s60, s52, s39
	global_load_lds_dwordx4 v[198:199], off
	v_lshl_add_u64 v[222:223], s[58:59], 0, v[132:133]
	s_mov_b32 m0, s60
	v_lshl_add_u64 v[224:225], s[36:37], 0, v[134:135]
	global_load_lds_dwordx4 v[222:223], off
	v_lshl_add_u64 v[222:223], s[58:59], 0, v[136:137]
	s_add_i32 m0, s60, 0x2000
	s_nop 0
	global_load_lds_dwordx4 v[222:223], off
	v_lshl_add_u64 v[222:223], s[36:37], 0, v[130:131]
	s_mov_b32 m0, s40
	s_nop 0
	global_load_lds_dwordx4 v[222:223], off
	s_mov_b32 m0, s41
	s_nop 0
	global_load_lds_dwordx4 v[224:225], off
	s_waitcnt vmcnt(8)
	s_waitcnt lgkmcnt(0)
	s_barrier
	s_setprio 1
	s_waitcnt lgkmcnt(0)
	v_mfma_f32_16x16x32_bf16 v[62:65], v[146:149], v[186:189], v[62:65]
	v_mfma_f32_16x16x32_bf16 v[58:61], v[162:165], v[186:189], v[58:61]
	v_mfma_f32_16x16x32_bf16 v[46:49], v[146:149], v[194:197], v[46:49]
	v_mfma_f32_16x16x32_bf16 v[42:45], v[162:165], v[194:197], v[42:45]
	v_mfma_f32_16x16x32_bf16 v[30:33], v[146:149], v[206:209], v[30:33]
	v_mfma_f32_16x16x32_bf16 v[26:29], v[162:165], v[206:209], v[26:29]
	v_mfma_f32_16x16x32_bf16 v[14:17], v[146:149], v[214:217], v[14:17]
	v_mfma_f32_16x16x32_bf16 v[10:13], v[162:165], v[214:217], v[10:13]
	v_mfma_f32_16x16x32_bf16 v[62:65], v[150:153], v[190:193], v[62:65]
	v_mfma_f32_16x16x32_bf16 v[58:61], v[166:169], v[190:193], v[58:61]
	v_mfma_f32_16x16x32_bf16 v[46:49], v[150:153], v[202:205], v[46:49]
	v_mfma_f32_16x16x32_bf16 v[42:45], v[166:169], v[202:205], v[42:45]
	v_mfma_f32_16x16x32_bf16 v[30:33], v[150:153], v[210:213], v[30:33]
	v_mfma_f32_16x16x32_bf16 v[26:29], v[166:169], v[210:213], v[26:29]
	v_mfma_f32_16x16x32_bf16 v[14:17], v[150:153], v[218:221], v[14:17]
	v_mfma_f32_16x16x32_bf16 v[10:13], v[166:169], v[218:221], v[10:13]
	s_setprio 0
	s_setprio 1
	v_mfma_f32_16x16x32_bf16 v[54:57], v[170:173], v[186:189], v[54:57]
	v_mfma_f32_16x16x32_bf16 v[50:53], v[178:181], v[186:189], v[50:53]
	v_mfma_f32_16x16x32_bf16 v[38:41], v[170:173], v[194:197], v[38:41]
	v_mfma_f32_16x16x32_bf16 v[34:37], v[178:181], v[194:197], v[34:37]
	v_mfma_f32_16x16x32_bf16 v[22:25], v[170:173], v[206:209], v[22:25]
	v_mfma_f32_16x16x32_bf16 v[18:21], v[178:181], v[206:209], v[18:21]
	v_mfma_f32_16x16x32_bf16 v[6:9], v[170:173], v[214:217], v[6:9]
	v_mfma_f32_16x16x32_bf16 v[2:5], v[178:181], v[214:217], v[2:5]
	v_mfma_f32_16x16x32_bf16 v[54:57], v[174:177], v[190:193], v[54:57]
	v_mfma_f32_16x16x32_bf16 v[50:53], v[182:185], v[190:193], v[50:53]
	v_mfma_f32_16x16x32_bf16 v[38:41], v[174:177], v[202:205], v[38:41]
	v_mfma_f32_16x16x32_bf16 v[34:37], v[182:185], v[202:205], v[34:37]
	v_mfma_f32_16x16x32_bf16 v[22:25], v[174:177], v[210:213], v[22:25]
	v_mfma_f32_16x16x32_bf16 v[18:21], v[182:185], v[210:213], v[18:21]
	v_mfma_f32_16x16x32_bf16 v[6:9], v[174:177], v[218:221], v[6:9]
	v_mfma_f32_16x16x32_bf16 v[2:5], v[182:185], v[218:221], v[2:5]
	s_setprio 0
	s_barrier
	s_add_i32 s58, 0, 0x18000
	s_add_i32 s59, 0, 0x1c000
	v_add_u32_e32 v166, s58, v156
	v_add_u32_e32 v182, s59, v156
	ds_read_b128 v[146:149], v166
	ds_read_b128 v[150:153], v166 offset:1024
	ds_read_b128 v[162:165], v166 offset:2048
	ds_read_b128 v[166:169], v166 offset:3072
	ds_read_b128 v[170:173], v182
	ds_read_b128 v[174:177], v182 offset:1024
	ds_read_b128 v[178:181], v182 offset:2048
	ds_read_b128 v[182:185], v182 offset:3072
	s_add_u32 s36, s36, 0x40000
	s_addc_u32 s37, s37, 0
	s_mov_b32 m0, s42
	v_lshl_add_u64 v[226:227], s[36:37], 0, v[130:131]
	ds_read_b128 v[186:189], v160 offset:32768
	ds_read_b128 v[190:193], v160 offset:33792
	ds_read_b128 v[194:197], v160 offset:34816
	ds_read_b128 v[202:205], v160 offset:35840
	ds_read_b128 v[206:209], v160 offset:36864
	ds_read_b128 v[210:213], v160 offset:37888
	ds_read_b128 v[214:217], v160 offset:38912
	ds_read_b128 v[218:221], v160 offset:39936
	global_load_lds_dwordx4 v[226:227], off
	v_lshl_add_u64 v[226:227], s[36:37], 0, v[134:135]
	s_mov_b32 m0, s43
	s_nop 0
	global_load_lds_dwordx4 v[226:227], off
	s_waitcnt vmcnt(8)
	s_waitcnt lgkmcnt(0)
	s_barrier
	s_setprio 1
	s_waitcnt lgkmcnt(0)
	v_mfma_f32_16x16x32_bf16 v[126:129], v[146:149], v[186:189], v[126:129]
	v_mfma_f32_16x16x32_bf16 v[122:125], v[162:165], v[186:189], v[122:125]
	v_mfma_f32_16x16x32_bf16 v[110:113], v[146:149], v[194:197], v[110:113]
	v_mfma_f32_16x16x32_bf16 v[106:109], v[162:165], v[194:197], v[106:109]
	v_mfma_f32_16x16x32_bf16 v[94:97], v[146:149], v[206:209], v[94:97]
	v_mfma_f32_16x16x32_bf16 v[90:93], v[162:165], v[206:209], v[90:93]
	v_mfma_f32_16x16x32_bf16 v[78:81], v[146:149], v[214:217], v[78:81]
	v_mfma_f32_16x16x32_bf16 v[74:77], v[162:165], v[214:217], v[74:77]
	v_mfma_f32_16x16x32_bf16 v[126:129], v[150:153], v[190:193], v[126:129]
	v_mfma_f32_16x16x32_bf16 v[122:125], v[166:169], v[190:193], v[122:125]
	v_mfma_f32_16x16x32_bf16 v[110:113], v[150:153], v[202:205], v[110:113]
	v_mfma_f32_16x16x32_bf16 v[106:109], v[166:169], v[202:205], v[106:109]
	v_mfma_f32_16x16x32_bf16 v[94:97], v[150:153], v[210:213], v[94:97]
	v_mfma_f32_16x16x32_bf16 v[90:93], v[166:169], v[210:213], v[90:93]
	v_mfma_f32_16x16x32_bf16 v[78:81], v[150:153], v[218:221], v[78:81]
	v_mfma_f32_16x16x32_bf16 v[74:77], v[166:169], v[218:221], v[74:77]
	s_setprio 0
	s_setprio 1
	v_mfma_f32_16x16x32_bf16 v[118:121], v[170:173], v[186:189], v[118:121]
	v_mfma_f32_16x16x32_bf16 v[114:117], v[178:181], v[186:189], v[114:117]
	v_mfma_f32_16x16x32_bf16 v[102:105], v[170:173], v[194:197], v[102:105]
	v_mfma_f32_16x16x32_bf16 v[98:101], v[178:181], v[194:197], v[98:101]
	v_mfma_f32_16x16x32_bf16 v[86:89], v[170:173], v[206:209], v[86:89]
	v_mfma_f32_16x16x32_bf16 v[82:85], v[178:181], v[206:209], v[82:85]
	v_mfma_f32_16x16x32_bf16 v[70:73], v[170:173], v[214:217], v[70:73]
	v_mfma_f32_16x16x32_bf16 v[66:69], v[178:181], v[214:217], v[66:69]
	v_mfma_f32_16x16x32_bf16 v[118:121], v[174:177], v[190:193], v[118:121]
	v_mfma_f32_16x16x32_bf16 v[114:117], v[182:185], v[190:193], v[114:117]
	v_mfma_f32_16x16x32_bf16 v[102:105], v[174:177], v[202:205], v[102:105]
	v_mfma_f32_16x16x32_bf16 v[98:101], v[182:185], v[202:205], v[98:101]
	v_mfma_f32_16x16x32_bf16 v[86:89], v[174:177], v[210:213], v[86:89]
	v_mfma_f32_16x16x32_bf16 v[82:85], v[182:185], v[210:213], v[82:85]
	v_mfma_f32_16x16x32_bf16 v[70:73], v[174:177], v[218:221], v[70:73]
	v_mfma_f32_16x16x32_bf16 v[66:69], v[182:185], v[218:221], v[66:69]
	s_setprio 0
	s_barrier
	s_add_i32 s36, s58, s39
	v_lshl_add_u64 v[154:155], v[154:155], 0, s[16:17]
	s_mov_b32 m0, s36
	ds_read_b128 v[186:189], v160 offset:49152
	ds_read_b128 v[190:193], v160 offset:50176
	ds_read_b128 v[194:197], v160 offset:51200
	ds_read_b128 v[202:205], v160 offset:52224
	ds_read_b128 v[206:209], v160 offset:53248
	ds_read_b128 v[210:213], v160 offset:54272
	ds_read_b128 v[214:217], v160 offset:55296
	ds_read_b128 v[218:221], v160 offset:56320
	global_load_lds_dwordx4 v[154:155], off
	s_add_i32 m0, s36, 0x2000
	s_add_u32 s34, s34, 0x40080
	v_lshl_add_u64 v[154:155], v[198:199], 0, s[16:17]
	s_addc_u32 s35, s35, 0
	s_add_i32 s36, s59, s39
	global_load_lds_dwordx4 v[154:155], off
	v_lshl_add_u64 v[154:155], s[34:35], 0, v[132:133]
	s_mov_b32 m0, s36
	s_nop 0
	global_load_lds_dwordx4 v[154:155], off
	v_lshl_add_u64 v[154:155], s[34:35], 0, v[136:137]
	s_add_i32 m0, s36, 0x2000
	s_nop 0
	global_load_lds_dwordx4 v[154:155], off
	v_lshl_add_u64 v[154:155], v[222:223], 0, s[16:17]
	s_mov_b32 m0, s47
	s_nop 0
	global_load_lds_dwordx4 v[154:155], off
	v_lshl_add_u64 v[154:155], v[224:225], 0, s[16:17]
	s_mov_b32 m0, s48
	s_nop 0
	global_load_lds_dwordx4 v[154:155], off
	s_waitcnt vmcnt(8)
	s_waitcnt lgkmcnt(0)
	s_barrier
	s_setprio 1
	s_waitcnt lgkmcnt(0)
	v_mfma_f32_16x16x32_bf16 v[62:65], v[146:149], v[186:189], v[62:65]
	v_mfma_f32_16x16x32_bf16 v[58:61], v[162:165], v[186:189], v[58:61]
	v_mfma_f32_16x16x32_bf16 v[46:49], v[146:149], v[194:197], v[46:49]
	v_mfma_f32_16x16x32_bf16 v[42:45], v[162:165], v[194:197], v[42:45]
	v_mfma_f32_16x16x32_bf16 v[30:33], v[146:149], v[206:209], v[30:33]
	v_mfma_f32_16x16x32_bf16 v[26:29], v[162:165], v[206:209], v[26:29]
	v_mfma_f32_16x16x32_bf16 v[14:17], v[146:149], v[214:217], v[14:17]
	v_mfma_f32_16x16x32_bf16 v[10:13], v[162:165], v[214:217], v[10:13]
	v_mfma_f32_16x16x32_bf16 v[62:65], v[150:153], v[190:193], v[62:65]
	v_mfma_f32_16x16x32_bf16 v[58:61], v[166:169], v[190:193], v[58:61]
	v_mfma_f32_16x16x32_bf16 v[46:49], v[150:153], v[202:205], v[46:49]
	v_mfma_f32_16x16x32_bf16 v[42:45], v[166:169], v[202:205], v[42:45]
	v_mfma_f32_16x16x32_bf16 v[30:33], v[150:153], v[210:213], v[30:33]
	v_mfma_f32_16x16x32_bf16 v[26:29], v[166:169], v[210:213], v[26:29]
	v_mfma_f32_16x16x32_bf16 v[14:17], v[150:153], v[218:221], v[14:17]
	v_mfma_f32_16x16x32_bf16 v[10:13], v[166:169], v[218:221], v[10:13]
	s_setprio 0
	s_setprio 1
	v_mfma_f32_16x16x32_bf16 v[54:57], v[170:173], v[186:189], v[54:57]
	v_mfma_f32_16x16x32_bf16 v[50:53], v[178:181], v[186:189], v[50:53]
	v_mfma_f32_16x16x32_bf16 v[38:41], v[170:173], v[194:197], v[38:41]
	v_mfma_f32_16x16x32_bf16 v[34:37], v[178:181], v[194:197], v[34:37]
	v_mfma_f32_16x16x32_bf16 v[22:25], v[170:173], v[206:209], v[22:25]
	v_mfma_f32_16x16x32_bf16 v[18:21], v[178:181], v[206:209], v[18:21]
	v_mfma_f32_16x16x32_bf16 v[6:9], v[170:173], v[214:217], v[6:9]
	v_mfma_f32_16x16x32_bf16 v[2:5], v[178:181], v[214:217], v[2:5]
	v_mfma_f32_16x16x32_bf16 v[54:57], v[174:177], v[190:193], v[54:57]
	v_mfma_f32_16x16x32_bf16 v[50:53], v[182:185], v[190:193], v[50:53]
	v_mfma_f32_16x16x32_bf16 v[38:41], v[174:177], v[202:205], v[38:41]
	v_mfma_f32_16x16x32_bf16 v[34:37], v[182:185], v[202:205], v[34:37]
	v_mfma_f32_16x16x32_bf16 v[22:25], v[174:177], v[210:213], v[22:25]
	v_mfma_f32_16x16x32_bf16 v[18:21], v[182:185], v[210:213], v[18:21]
	v_mfma_f32_16x16x32_bf16 v[6:9], v[174:177], v[218:221], v[6:9]
	v_mfma_f32_16x16x32_bf16 v[2:5], v[182:185], v[218:221], v[2:5]
	s_setprio 0
	s_add_i32 s57, s57, 2
	s_add_u32 s30, s30, 0x100
	s_addc_u32 s31, s31, 0
	s_add_u32 s55, s55, 0x100
	s_addc_u32 s56, s56, 0
	s_cmp_gt_u32 s57, 13
	s_barrier
	s_cbranch_scc0 .LBB0_1640
	s_and_b64 vcc, exec, s[18:19]
	s_cbranch_vccz .LBB0_1643
	s_barrier

.LBB0_1741:
	ds_read_b128 v[58:61], v172
	ds_read_b128 v[62:65], v172 offset:1024
	ds_read_b128 v[74:77], v172 offset:2048
	ds_read_b128 v[78:81], v172 offset:3072
	ds_read_b128 v[166:169], v173
	ds_read_b128 v[176:179], v173 offset:1024
	ds_read_b128 v[180:183], v173 offset:2048
	ds_read_b128 v[184:187], v173 offset:3072
	s_add_u32 s28, s26, 0xfffc0080
	s_addc_u32 s29, s27, -1
	s_cmp_eq_u32 s56, 12
	s_cselect_b32 s31, s17, s29
	s_cselect_b32 s30, s23, s28
	s_cselect_b32 s29, s15, s55
	s_cselect_b32 s28, s25, s54
	v_lshl_add_u64 v[222:223], s[26:27], 0, v[158:159]
	s_add_i32 m0, s39, 0xc000
	ds_read_b128 v[188:191], v174
	ds_read_b128 v[192:195], v174 offset:1024
	ds_read_b128 v[196:199], v174 offset:2048
	ds_read_b128 v[202:205], v174 offset:3072
	ds_read_b128 v[206:209], v174 offset:4096
	ds_read_b128 v[210:213], v174 offset:5120
	ds_read_b128 v[214:217], v174 offset:6144
	ds_read_b128 v[218:221], v174 offset:7168
	global_load_lds_dwordx4 v[222:223], off
	v_lshl_add_u64 v[222:223], s[26:27], 0, v[160:161]
	s_add_i32 m0, s39, 0xe000
	s_nop 0
	global_load_lds_dwordx4 v[222:223], off
	s_waitcnt vmcnt(8)
	s_waitcnt lgkmcnt(0)
	s_barrier
	s_setprio 1
	s_waitcnt lgkmcnt(0)
	v_mfma_f32_16x16x32_bf16 v[142:145], v[58:61], v[188:191], v[142:145]
	v_mfma_f32_16x16x32_bf16 v[138:141], v[74:77], v[188:191], v[138:141]
	v_mfma_f32_16x16x32_bf16 v[126:129], v[58:61], v[196:199], v[126:129]
	v_mfma_f32_16x16x32_bf16 v[122:125], v[74:77], v[196:199], v[122:125]
	v_mfma_f32_16x16x32_bf16 v[110:113], v[58:61], v[206:209], v[110:113]
	v_mfma_f32_16x16x32_bf16 v[106:109], v[74:77], v[206:209], v[106:109]
	v_mfma_f32_16x16x32_bf16 v[94:97], v[58:61], v[214:217], v[94:97]
	v_mfma_f32_16x16x32_bf16 v[90:93], v[74:77], v[214:217], v[90:93]
	v_mfma_f32_16x16x32_bf16 v[142:145], v[62:65], v[192:195], v[142:145]
	v_mfma_f32_16x16x32_bf16 v[138:141], v[78:81], v[192:195], v[138:141]
	v_mfma_f32_16x16x32_bf16 v[126:129], v[62:65], v[202:205], v[126:129]
	v_mfma_f32_16x16x32_bf16 v[122:125], v[78:81], v[202:205], v[122:125]
	v_mfma_f32_16x16x32_bf16 v[110:113], v[62:65], v[210:213], v[110:113]
	v_mfma_f32_16x16x32_bf16 v[106:109], v[78:81], v[210:213], v[106:109]
	v_mfma_f32_16x16x32_bf16 v[94:97], v[62:65], v[218:221], v[94:97]
	v_mfma_f32_16x16x32_bf16 v[90:93], v[78:81], v[218:221], v[90:93]
	s_setprio 0
	s_setprio 1
	v_mfma_f32_16x16x32_bf16 v[134:137], v[166:169], v[188:191], v[134:137]
	v_mfma_f32_16x16x32_bf16 v[130:133], v[180:183], v[188:191], v[130:133]
	v_mfma_f32_16x16x32_bf16 v[118:121], v[166:169], v[196:199], v[118:121]
	v_mfma_f32_16x16x32_bf16 v[114:117], v[180:183], v[196:199], v[114:117]
	v_mfma_f32_16x16x32_bf16 v[102:105], v[166:169], v[206:209], v[102:105]
	v_mfma_f32_16x16x32_bf16 v[98:101], v[180:183], v[206:209], v[98:101]
	v_mfma_f32_16x16x32_bf16 v[86:89], v[166:169], v[214:217], v[86:89]
	v_mfma_f32_16x16x32_bf16 v[82:85], v[180:183], v[214:217], v[82:85]
	v_mfma_f32_16x16x32_bf16 v[134:137], v[176:179], v[192:195], v[134:137]
	v_mfma_f32_16x16x32_bf16 v[130:133], v[184:187], v[192:195], v[130:133]
	v_mfma_f32_16x16x32_bf16 v[118:121], v[176:179], v[202:205], v[118:121]
	v_mfma_f32_16x16x32_bf16 v[114:117], v[184:187], v[202:205], v[114:117]
	v_mfma_f32_16x16x32_bf16 v[102:105], v[176:179], v[210:213], v[102:105]
	v_mfma_f32_16x16x32_bf16 v[98:101], v[184:187], v[210:213], v[98:101]
	v_mfma_f32_16x16x32_bf16 v[86:89], v[176:179], v[218:221], v[86:89]
	v_mfma_f32_16x16x32_bf16 v[82:85], v[184:187], v[218:221], v[82:85]
	s_setprio 0
	s_barrier
	s_add_i32 s57, s51, s34
	v_lshl_add_u64 v[222:223], s[28:29], 0, v[148:149]
	s_mov_b32 m0, s57
	ds_read_b128 v[188:191], v174 offset:16384
	ds_read_b128 v[192:195], v174 offset:17408
	ds_read_b128 v[196:199], v174 offset:18432
	ds_read_b128 v[202:205], v174 offset:19456
	ds_read_b128 v[206:209], v174 offset:20480
	ds_read_b128 v[210:213], v174 offset:21504
	ds_read_b128 v[214:217], v174 offset:22528
	ds_read_b128 v[218:221], v174 offset:23552
	global_load_lds_dwordx4 v[222:223], off
	s_add_i32 m0, s57, 0x2000
	s_add_u32 s58, s28, 0x40000
	v_lshl_add_u64 v[224:225], s[28:29], 0, v[152:153]
	s_addc_u32 s59, s29, 0
	s_add_i32 s57, s52, s34
	global_load_lds_dwordx4 v[224:225], off
	v_lshl_add_u64 v[226:227], s[58:59], 0, v[148:149]
	s_mov_b32 m0, s57
	v_lshl_add_u64 v[228:229], s[30:31], 0, v[150:151]
	global_load_lds_dwordx4 v[226:227], off
	v_lshl_add_u64 v[226:227], s[58:59], 0, v[152:153]
	s_add_i32 m0, s57, 0x2000
	s_nop 0
	global_load_lds_dwordx4 v[226:227], off
	v_lshl_add_u64 v[226:227], s[30:31], 0, v[146:147]
	s_mov_b32 m0, s39
	s_nop 0
	global_load_lds_dwordx4 v[226:227], off
	s_mov_b32 m0, s40
	s_nop 0
	global_load_lds_dwordx4 v[228:229], off
	s_waitcnt vmcnt(8)
	s_waitcnt lgkmcnt(0)
	s_barrier
	s_setprio 1
	s_waitcnt lgkmcnt(0)
	v_mfma_f32_16x16x32_bf16 v[70:73], v[58:61], v[188:191], v[70:73]
	v_mfma_f32_16x16x32_bf16 v[66:69], v[74:77], v[188:191], v[66:69]
	v_mfma_f32_16x16x32_bf16 v[46:49], v[58:61], v[196:199], v[46:49]
	v_mfma_f32_16x16x32_bf16 v[42:45], v[74:77], v[196:199], v[42:45]
	v_mfma_f32_16x16x32_bf16 v[30:33], v[58:61], v[206:209], v[30:33]
	v_mfma_f32_16x16x32_bf16 v[26:29], v[74:77], v[206:209], v[26:29]
	v_mfma_f32_16x16x32_bf16 v[14:17], v[58:61], v[214:217], v[14:17]
	v_mfma_f32_16x16x32_bf16 v[10:13], v[74:77], v[214:217], v[10:13]
	v_mfma_f32_16x16x32_bf16 v[70:73], v[62:65], v[192:195], v[70:73]
	v_mfma_f32_16x16x32_bf16 v[66:69], v[78:81], v[192:195], v[66:69]
	v_mfma_f32_16x16x32_bf16 v[46:49], v[62:65], v[202:205], v[46:49]
	v_mfma_f32_16x16x32_bf16 v[42:45], v[78:81], v[202:205], v[42:45]
	v_mfma_f32_16x16x32_bf16 v[30:33], v[62:65], v[210:213], v[30:33]
	v_mfma_f32_16x16x32_bf16 v[26:29], v[78:81], v[210:213], v[26:29]
	v_mfma_f32_16x16x32_bf16 v[14:17], v[62:65], v[218:221], v[14:17]
	v_mfma_f32_16x16x32_bf16 v[10:13], v[78:81], v[218:221], v[10:13]
	s_setprio 0
	s_setprio 1
	v_mfma_f32_16x16x32_bf16 v[54:57], v[166:169], v[188:191], v[54:57]
	v_mfma_f32_16x16x32_bf16 v[50:53], v[180:183], v[188:191], v[50:53]
	v_mfma_f32_16x16x32_bf16 v[38:41], v[166:169], v[196:199], v[38:41]
	v_mfma_f32_16x16x32_bf16 v[34:37], v[180:183], v[196:199], v[34:37]
	v_mfma_f32_16x16x32_bf16 v[22:25], v[166:169], v[206:209], v[22:25]
	v_mfma_f32_16x16x32_bf16 v[18:21], v[180:183], v[206:209], v[18:21]
	v_mfma_f32_16x16x32_bf16 v[6:9], v[166:169], v[214:217], v[6:9]
	v_mfma_f32_16x16x32_bf16 v[2:5], v[180:183], v[214:217], v[2:5]
	v_mfma_f32_16x16x32_bf16 v[54:57], v[176:179], v[192:195], v[54:57]
	v_mfma_f32_16x16x32_bf16 v[50:53], v[184:187], v[192:195], v[50:53]
	v_mfma_f32_16x16x32_bf16 v[38:41], v[176:179], v[202:205], v[38:41]
	v_mfma_f32_16x16x32_bf16 v[34:37], v[184:187], v[202:205], v[34:37]
	v_mfma_f32_16x16x32_bf16 v[22:25], v[176:179], v[210:213], v[22:25]
	v_mfma_f32_16x16x32_bf16 v[18:21], v[184:187], v[210:213], v[18:21]
	v_mfma_f32_16x16x32_bf16 v[6:9], v[176:179], v[218:221], v[6:9]
	v_mfma_f32_16x16x32_bf16 v[2:5], v[184:187], v[218:221], v[2:5]
	s_setprio 0
	s_barrier
	s_add_i32 s57, 0, 0x18000
	s_add_i32 s58, 0, 0x1c000
	v_add_u32_e32 v78, s57, v157
	v_add_u32_e32 v184, s58, v157
	ds_read_b128 v[58:61], v78
	ds_read_b128 v[62:65], v78 offset:1024
	ds_read_b128 v[74:77], v78 offset:2048
	ds_read_b128 v[78:81], v78 offset:3072
	ds_read_b128 v[166:169], v184
	ds_read_b128 v[176:179], v184 offset:1024
	ds_read_b128 v[180:183], v184 offset:2048
	ds_read_b128 v[184:187], v184 offset:3072
	s_add_u32 s30, s30, 0x40000
	s_addc_u32 s31, s31, 0
	s_mov_b32 m0, s41
	v_lshl_add_u64 v[230:231], s[30:31], 0, v[146:147]
	ds_read_b128 v[188:191], v174 offset:32768
	ds_read_b128 v[192:195], v174 offset:33792
	ds_read_b128 v[196:199], v174 offset:34816
	ds_read_b128 v[202:205], v174 offset:35840
	ds_read_b128 v[206:209], v174 offset:36864
	ds_read_b128 v[210:213], v174 offset:37888
	ds_read_b128 v[214:217], v174 offset:38912
	ds_read_b128 v[218:221], v174 offset:39936
	global_load_lds_dwordx4 v[230:231], off
	v_lshl_add_u64 v[230:231], s[30:31], 0, v[150:151]
	s_mov_b32 m0, s42
	s_nop 0
	global_load_lds_dwordx4 v[230:231], off
	s_waitcnt vmcnt(8)
	s_waitcnt lgkmcnt(0)
	s_barrier
	s_setprio 1
	s_waitcnt lgkmcnt(0)
	v_mfma_f32_16x16x32_bf16 v[142:145], v[58:61], v[188:191], v[142:145]
	v_mfma_f32_16x16x32_bf16 v[138:141], v[74:77], v[188:191], v[138:141]
	v_mfma_f32_16x16x32_bf16 v[126:129], v[58:61], v[196:199], v[126:129]
	v_mfma_f32_16x16x32_bf16 v[122:125], v[74:77], v[196:199], v[122:125]
	v_mfma_f32_16x16x32_bf16 v[110:113], v[58:61], v[206:209], v[110:113]
	v_mfma_f32_16x16x32_bf16 v[106:109], v[74:77], v[206:209], v[106:109]
	v_mfma_f32_16x16x32_bf16 v[94:97], v[58:61], v[214:217], v[94:97]
	v_mfma_f32_16x16x32_bf16 v[90:93], v[74:77], v[214:217], v[90:93]
	v_mfma_f32_16x16x32_bf16 v[142:145], v[62:65], v[192:195], v[142:145]
	v_mfma_f32_16x16x32_bf16 v[138:141], v[78:81], v[192:195], v[138:141]
	v_mfma_f32_16x16x32_bf16 v[126:129], v[62:65], v[202:205], v[126:129]
	v_mfma_f32_16x16x32_bf16 v[122:125], v[78:81], v[202:205], v[122:125]
	v_mfma_f32_16x16x32_bf16 v[110:113], v[62:65], v[210:213], v[110:113]
	v_mfma_f32_16x16x32_bf16 v[106:109], v[78:81], v[210:213], v[106:109]
	v_mfma_f32_16x16x32_bf16 v[94:97], v[62:65], v[218:221], v[94:97]
	v_mfma_f32_16x16x32_bf16 v[90:93], v[78:81], v[218:221], v[90:93]
	s_setprio 0
	s_setprio 1
	v_mfma_f32_16x16x32_bf16 v[134:137], v[166:169], v[188:191], v[134:137]
	v_mfma_f32_16x16x32_bf16 v[130:133], v[180:183], v[188:191], v[130:133]
	v_mfma_f32_16x16x32_bf16 v[118:121], v[166:169], v[196:199], v[118:121]
	v_mfma_f32_16x16x32_bf16 v[114:117], v[180:183], v[196:199], v[114:117]
	v_mfma_f32_16x16x32_bf16 v[102:105], v[166:169], v[206:209], v[102:105]
	v_mfma_f32_16x16x32_bf16 v[98:101], v[180:183], v[206:209], v[98:101]
	v_mfma_f32_16x16x32_bf16 v[86:89], v[166:169], v[214:217], v[86:89]
	v_mfma_f32_16x16x32_bf16 v[82:85], v[180:183], v[214:217], v[82:85]
	v_mfma_f32_16x16x32_bf16 v[134:137], v[176:179], v[192:195], v[134:137]
	v_mfma_f32_16x16x32_bf16 v[130:133], v[184:187], v[192:195], v[130:133]
	v_mfma_f32_16x16x32_bf16 v[118:121], v[176:179], v[202:205], v[118:121]
	v_mfma_f32_16x16x32_bf16 v[114:117], v[184:187], v[202:205], v[114:117]
	v_mfma_f32_16x16x32_bf16 v[102:105], v[176:179], v[210:213], v[102:105]
	v_mfma_f32_16x16x32_bf16 v[98:101], v[184:187], v[210:213], v[98:101]
	v_mfma_f32_16x16x32_bf16 v[86:89], v[176:179], v[218:221], v[86:89]
	v_mfma_f32_16x16x32_bf16 v[82:85], v[184:187], v[218:221], v[82:85]
	s_setprio 0
	s_barrier
	s_add_i32 s30, s57, s34
	v_lshl_add_u64 v[222:223], v[222:223], 0, s[10:11]
	s_mov_b32 m0, s30
	ds_read_b128 v[188:191], v174 offset:49152
	ds_read_b128 v[192:195], v174 offset:50176
	ds_read_b128 v[196:199], v174 offset:51200
	ds_read_b128 v[202:205], v174 offset:52224
	ds_read_b128 v[206:209], v174 offset:53248
	ds_read_b128 v[210:213], v174 offset:54272
	ds_read_b128 v[214:217], v174 offset:55296
	ds_read_b128 v[218:221], v174 offset:56320
	global_load_lds_dwordx4 v[222:223], off
	s_add_i32 m0, s30, 0x2000
	s_add_u32 s28, s28, 0x40080
	v_lshl_add_u64 v[222:223], v[224:225], 0, s[10:11]
	s_addc_u32 s29, s29, 0
	s_add_i32 s30, s58, s34
	global_load_lds_dwordx4 v[222:223], off
	v_lshl_add_u64 v[222:223], s[28:29], 0, v[148:149]
	s_mov_b32 m0, s30
	s_nop 0
	global_load_lds_dwordx4 v[222:223], off
	v_lshl_add_u64 v[222:223], s[28:29], 0, v[152:153]
	s_add_i32 m0, s30, 0x2000
	s_nop 0
	global_load_lds_dwordx4 v[222:223], off
	v_lshl_add_u64 v[222:223], v[226:227], 0, s[10:11]
	s_mov_b32 m0, s46
	s_nop 0
	global_load_lds_dwordx4 v[222:223], off
	v_lshl_add_u64 v[222:223], v[228:229], 0, s[10:11]
	s_mov_b32 m0, s47
	s_nop 0
	global_load_lds_dwordx4 v[222:223], off
	s_waitcnt vmcnt(8)
	s_waitcnt lgkmcnt(0)
	s_barrier
	s_setprio 1
	s_waitcnt lgkmcnt(0)
	v_mfma_f32_16x16x32_bf16 v[70:73], v[58:61], v[188:191], v[70:73]
	v_mfma_f32_16x16x32_bf16 v[66:69], v[74:77], v[188:191], v[66:69]
	v_mfma_f32_16x16x32_bf16 v[46:49], v[58:61], v[196:199], v[46:49]
	v_mfma_f32_16x16x32_bf16 v[42:45], v[74:77], v[196:199], v[42:45]
	v_mfma_f32_16x16x32_bf16 v[30:33], v[58:61], v[206:209], v[30:33]
	v_mfma_f32_16x16x32_bf16 v[26:29], v[74:77], v[206:209], v[26:29]
	v_mfma_f32_16x16x32_bf16 v[14:17], v[58:61], v[214:217], v[14:17]
	v_mfma_f32_16x16x32_bf16 v[10:13], v[74:77], v[214:217], v[10:13]
	v_mfma_f32_16x16x32_bf16 v[70:73], v[62:65], v[192:195], v[70:73]
	v_mfma_f32_16x16x32_bf16 v[66:69], v[78:81], v[192:195], v[66:69]
	v_mfma_f32_16x16x32_bf16 v[46:49], v[62:65], v[202:205], v[46:49]
	v_mfma_f32_16x16x32_bf16 v[42:45], v[78:81], v[202:205], v[42:45]
	v_mfma_f32_16x16x32_bf16 v[30:33], v[62:65], v[210:213], v[30:33]
	v_mfma_f32_16x16x32_bf16 v[26:29], v[78:81], v[210:213], v[26:29]
	v_mfma_f32_16x16x32_bf16 v[14:17], v[62:65], v[218:221], v[14:17]
	v_mfma_f32_16x16x32_bf16 v[10:13], v[78:81], v[218:221], v[10:13]
	s_setprio 0
	s_setprio 1
	v_mfma_f32_16x16x32_bf16 v[54:57], v[166:169], v[188:191], v[54:57]
	v_mfma_f32_16x16x32_bf16 v[50:53], v[180:183], v[188:191], v[50:53]
	v_mfma_f32_16x16x32_bf16 v[38:41], v[166:169], v[196:199], v[38:41]
	v_mfma_f32_16x16x32_bf16 v[34:37], v[180:183], v[196:199], v[34:37]
	v_mfma_f32_16x16x32_bf16 v[22:25], v[166:169], v[206:209], v[22:25]
	v_mfma_f32_16x16x32_bf16 v[18:21], v[180:183], v[206:209], v[18:21]
	v_mfma_f32_16x16x32_bf16 v[6:9], v[166:169], v[214:217], v[6:9]
	v_mfma_f32_16x16x32_bf16 v[2:5], v[180:183], v[214:217], v[2:5]
	v_mfma_f32_16x16x32_bf16 v[54:57], v[176:179], v[192:195], v[54:57]
	v_mfma_f32_16x16x32_bf16 v[50:53], v[184:187], v[192:195], v[50:53]
	v_mfma_f32_16x16x32_bf16 v[38:41], v[176:179], v[202:205], v[38:41]
	v_mfma_f32_16x16x32_bf16 v[34:37], v[184:187], v[202:205], v[34:37]
	v_mfma_f32_16x16x32_bf16 v[22:25], v[176:179], v[210:213], v[22:25]
	v_mfma_f32_16x16x32_bf16 v[18:21], v[184:187], v[210:213], v[18:21]
	v_mfma_f32_16x16x32_bf16 v[6:9], v[176:179], v[218:221], v[6:9]
	v_mfma_f32_16x16x32_bf16 v[2:5], v[184:187], v[218:221], v[2:5]
	s_setprio 0
	s_add_i32 s56, s56, 2
	s_add_u32 s26, s26, 0x100
	s_addc_u32 s27, s27, 0
	s_add_u32 s54, s54, 0x100
	s_addc_u32 s55, s55, 0
	s_cmp_gt_u32 s56, 13
	s_barrier
	s_cbranch_scc0 .LBB0_1741
	s_and_b64 vcc, exec, s[12:13]
	s_cbranch_vccz .LBB0_1744
	s_barrier

.LBB0_1858:
	ds_read_b128 v[144:147], v153
	ds_read_b128 v[158:161], v153 offset:1024
	ds_read_b128 v[162:165], v153 offset:2048
	ds_read_b128 v[166:169], v153 offset:3072
	ds_read_b128 v[170:173], v154
	ds_read_b128 v[174:177], v154 offset:1024
	ds_read_b128 v[178:181], v154 offset:2048
	ds_read_b128 v[182:185], v154 offset:3072
	s_add_u32 s26, s24, 0xfff50080
	s_addc_u32 s27, s25, -1
	s_cmp_eq_u32 s51, 40
	s_cselect_b32 s29, s9, s27
	s_cselect_b32 s28, s8, s26
	s_cselect_b32 s27, s23, s50
	s_cselect_b32 s26, s22, s0
	v_lshl_add_u64 v[148:149], s[24:25], 0, v[136:137]
	s_add_i32 m0, s34, 0xc000
	ds_read_b128 v[186:189], v155
	ds_read_b128 v[190:193], v155 offset:1024
	ds_read_b128 v[194:197], v155 offset:2048
	ds_read_b128 v[202:205], v155 offset:3072
	ds_read_b128 v[206:209], v155 offset:4096
	ds_read_b128 v[210:213], v155 offset:5120
	ds_read_b128 v[214:217], v155 offset:6144
	ds_read_b128 v[218:221], v155 offset:7168
	global_load_lds_dwordx4 v[148:149], off
	v_lshl_add_u64 v[148:149], s[24:25], 0, v[138:139]
	s_add_i32 m0, s34, 0xe000
	s_nop 0
	global_load_lds_dwordx4 v[148:149], off
	s_waitcnt vmcnt(8)
	s_waitcnt lgkmcnt(0)
	s_barrier
	s_setprio 1
	s_waitcnt lgkmcnt(0)
	v_mfma_f32_16x16x32_bf16 v[124:127], v[144:147], v[186:189], v[124:127]
	v_mfma_f32_16x16x32_bf16 v[120:123], v[162:165], v[186:189], v[120:123]
	v_mfma_f32_16x16x32_bf16 v[108:111], v[144:147], v[194:197], v[108:111]
	v_mfma_f32_16x16x32_bf16 v[104:107], v[162:165], v[194:197], v[104:107]
	v_mfma_f32_16x16x32_bf16 v[92:95], v[144:147], v[206:209], v[92:95]
	v_mfma_f32_16x16x32_bf16 v[88:91], v[162:165], v[206:209], v[88:91]
	v_mfma_f32_16x16x32_bf16 v[76:79], v[144:147], v[214:217], v[76:79]
	v_mfma_f32_16x16x32_bf16 v[72:75], v[162:165], v[214:217], v[72:75]
	v_mfma_f32_16x16x32_bf16 v[124:127], v[158:161], v[190:193], v[124:127]
	v_mfma_f32_16x16x32_bf16 v[120:123], v[166:169], v[190:193], v[120:123]
	v_mfma_f32_16x16x32_bf16 v[108:111], v[158:161], v[202:205], v[108:111]
	v_mfma_f32_16x16x32_bf16 v[104:107], v[166:169], v[202:205], v[104:107]
	v_mfma_f32_16x16x32_bf16 v[92:95], v[158:161], v[210:213], v[92:95]
	v_mfma_f32_16x16x32_bf16 v[88:91], v[166:169], v[210:213], v[88:91]
	v_mfma_f32_16x16x32_bf16 v[76:79], v[158:161], v[218:221], v[76:79]
	v_mfma_f32_16x16x32_bf16 v[72:75], v[166:169], v[218:221], v[72:75]
	s_setprio 0
	s_setprio 1
	v_mfma_f32_16x16x32_bf16 v[116:119], v[170:173], v[186:189], v[116:119]
	v_mfma_f32_16x16x32_bf16 v[112:115], v[178:181], v[186:189], v[112:115]
	v_mfma_f32_16x16x32_bf16 v[100:103], v[170:173], v[194:197], v[100:103]
	v_mfma_f32_16x16x32_bf16 v[96:99], v[178:181], v[194:197], v[96:99]
	v_mfma_f32_16x16x32_bf16 v[84:87], v[170:173], v[206:209], v[84:87]
	v_mfma_f32_16x16x32_bf16 v[80:83], v[178:181], v[206:209], v[80:83]
	v_mfma_f32_16x16x32_bf16 v[68:71], v[170:173], v[214:217], v[68:71]
	v_mfma_f32_16x16x32_bf16 v[64:67], v[178:181], v[214:217], v[64:67]
	v_mfma_f32_16x16x32_bf16 v[116:119], v[174:177], v[190:193], v[116:119]
	v_mfma_f32_16x16x32_bf16 v[112:115], v[182:185], v[190:193], v[112:115]
	v_mfma_f32_16x16x32_bf16 v[100:103], v[174:177], v[202:205], v[100:103]
	v_mfma_f32_16x16x32_bf16 v[96:99], v[182:185], v[202:205], v[96:99]
	v_mfma_f32_16x16x32_bf16 v[84:87], v[174:177], v[210:213], v[84:87]
	v_mfma_f32_16x16x32_bf16 v[80:83], v[182:185], v[210:213], v[80:83]
	v_mfma_f32_16x16x32_bf16 v[68:71], v[174:177], v[218:221], v[68:71]
	v_mfma_f32_16x16x32_bf16 v[64:67], v[182:185], v[218:221], v[64:67]
	s_setprio 0
	s_barrier
	s_add_i32 s52, s43, s33
	v_lshl_add_u64 v[148:149], s[26:27], 0, v[130:131]
	s_mov_b32 m0, s52
	ds_read_b128 v[186:189], v155 offset:16384
	ds_read_b128 v[190:193], v155 offset:17408
	ds_read_b128 v[194:197], v155 offset:18432
	ds_read_b128 v[202:205], v155 offset:19456
	ds_read_b128 v[206:209], v155 offset:20480
	ds_read_b128 v[210:213], v155 offset:21504
	ds_read_b128 v[214:217], v155 offset:22528
	ds_read_b128 v[218:221], v155 offset:23552
	global_load_lds_dwordx4 v[148:149], off
	s_add_i32 m0, s52, 0x2000
	s_add_u32 s52, s26, 0xb0000
	v_lshl_add_u64 v[198:199], s[26:27], 0, v[134:135]
	s_addc_u32 s53, s27, 0
	s_add_i32 s54, s44, s33
	global_load_lds_dwordx4 v[198:199], off
	v_lshl_add_u64 v[222:223], s[52:53], 0, v[130:131]
	s_mov_b32 m0, s54
	v_lshl_add_u64 v[224:225], s[28:29], 0, v[132:133]
	global_load_lds_dwordx4 v[222:223], off
	v_lshl_add_u64 v[222:223], s[52:53], 0, v[134:135]
	s_add_i32 m0, s54, 0x2000
	s_nop 0
	global_load_lds_dwordx4 v[222:223], off
	v_lshl_add_u64 v[222:223], s[28:29], 0, v[128:129]
	s_mov_b32 m0, s34
	s_nop 0
	global_load_lds_dwordx4 v[222:223], off
	s_mov_b32 m0, s35
	s_nop 0
	global_load_lds_dwordx4 v[224:225], off
	s_waitcnt vmcnt(8)
	s_waitcnt lgkmcnt(0)
	s_barrier
	s_setprio 1
	s_waitcnt lgkmcnt(0)
	v_mfma_f32_16x16x32_bf16 v[60:63], v[144:147], v[186:189], v[60:63]
	v_mfma_f32_16x16x32_bf16 v[56:59], v[162:165], v[186:189], v[56:59]
	v_mfma_f32_16x16x32_bf16 v[44:47], v[144:147], v[194:197], v[44:47]
	v_mfma_f32_16x16x32_bf16 v[40:43], v[162:165], v[194:197], v[40:43]
	v_mfma_f32_16x16x32_bf16 v[28:31], v[144:147], v[206:209], v[28:31]
	v_mfma_f32_16x16x32_bf16 v[24:27], v[162:165], v[206:209], v[24:27]
	v_mfma_f32_16x16x32_bf16 v[12:15], v[144:147], v[214:217], v[12:15]
	v_mfma_f32_16x16x32_bf16 v[8:11], v[162:165], v[214:217], v[8:11]
	v_mfma_f32_16x16x32_bf16 v[60:63], v[158:161], v[190:193], v[60:63]
	v_mfma_f32_16x16x32_bf16 v[56:59], v[166:169], v[190:193], v[56:59]
	v_mfma_f32_16x16x32_bf16 v[44:47], v[158:161], v[202:205], v[44:47]
	v_mfma_f32_16x16x32_bf16 v[40:43], v[166:169], v[202:205], v[40:43]
	v_mfma_f32_16x16x32_bf16 v[28:31], v[158:161], v[210:213], v[28:31]
	v_mfma_f32_16x16x32_bf16 v[24:27], v[166:169], v[210:213], v[24:27]
	v_mfma_f32_16x16x32_bf16 v[12:15], v[158:161], v[218:221], v[12:15]
	v_mfma_f32_16x16x32_bf16 v[8:11], v[166:169], v[218:221], v[8:11]
	s_setprio 0
	s_setprio 1
	v_mfma_f32_16x16x32_bf16 v[52:55], v[170:173], v[186:189], v[52:55]
	v_mfma_f32_16x16x32_bf16 v[48:51], v[178:181], v[186:189], v[48:51]
	v_mfma_f32_16x16x32_bf16 v[36:39], v[170:173], v[194:197], v[36:39]
	v_mfma_f32_16x16x32_bf16 v[32:35], v[178:181], v[194:197], v[32:35]
	v_mfma_f32_16x16x32_bf16 v[20:23], v[170:173], v[206:209], v[20:23]
	v_mfma_f32_16x16x32_bf16 v[16:19], v[178:181], v[206:209], v[16:19]
	v_mfma_f32_16x16x32_bf16 v[4:7], v[170:173], v[214:217], v[4:7]
	v_mfma_f32_16x16x32_bf16 v[0:3], v[178:181], v[214:217], v[0:3]
	v_mfma_f32_16x16x32_bf16 v[52:55], v[174:177], v[190:193], v[52:55]
	v_mfma_f32_16x16x32_bf16 v[48:51], v[182:185], v[190:193], v[48:51]
	v_mfma_f32_16x16x32_bf16 v[36:39], v[174:177], v[202:205], v[36:39]
	v_mfma_f32_16x16x32_bf16 v[32:35], v[182:185], v[202:205], v[32:35]
	v_mfma_f32_16x16x32_bf16 v[20:23], v[174:177], v[210:213], v[20:23]
	v_mfma_f32_16x16x32_bf16 v[16:19], v[182:185], v[210:213], v[16:19]
	v_mfma_f32_16x16x32_bf16 v[4:7], v[174:177], v[218:221], v[4:7]
	v_mfma_f32_16x16x32_bf16 v[0:3], v[182:185], v[218:221], v[0:3]
	s_setprio 0
	s_barrier
	s_add_i32 s52, 0, 0x18000
	v_add_u32_e32 v157, s52, v151
	s_add_i32 s53, 0, 0x1c000
	ds_read_b128 v[144:147], v157
	ds_read_b128 v[158:161], v157 offset:1024
	ds_read_b128 v[162:165], v157 offset:2048
	ds_read_b128 v[166:169], v157 offset:3072
	v_add_u32_e32 v157, s53, v151
	ds_read_b128 v[170:173], v157
	ds_read_b128 v[174:177], v157 offset:1024
	ds_read_b128 v[178:181], v157 offset:2048
	ds_read_b128 v[182:185], v157 offset:3072
	s_add_u32 s28, s28, 0xb0000
	s_addc_u32 s29, s29, 0
	s_mov_b32 m0, s36
	v_lshl_add_u64 v[226:227], s[28:29], 0, v[128:129]
	ds_read_b128 v[186:189], v155 offset:32768
	ds_read_b128 v[190:193], v155 offset:33792
	ds_read_b128 v[194:197], v155 offset:34816
	ds_read_b128 v[202:205], v155 offset:35840
	ds_read_b128 v[206:209], v155 offset:36864
	ds_read_b128 v[210:213], v155 offset:37888
	ds_read_b128 v[214:217], v155 offset:38912
	ds_read_b128 v[218:221], v155 offset:39936
	global_load_lds_dwordx4 v[226:227], off
	v_lshl_add_u64 v[226:227], s[28:29], 0, v[132:133]
	s_mov_b32 m0, s37
	s_nop 0
	global_load_lds_dwordx4 v[226:227], off
	s_waitcnt vmcnt(8)
	s_waitcnt lgkmcnt(0)
	s_barrier
	s_setprio 1
	s_waitcnt lgkmcnt(0)
	v_mfma_f32_16x16x32_bf16 v[124:127], v[144:147], v[186:189], v[124:127]
	v_mfma_f32_16x16x32_bf16 v[120:123], v[162:165], v[186:189], v[120:123]
	v_mfma_f32_16x16x32_bf16 v[108:111], v[144:147], v[194:197], v[108:111]
	v_mfma_f32_16x16x32_bf16 v[104:107], v[162:165], v[194:197], v[104:107]
	v_mfma_f32_16x16x32_bf16 v[92:95], v[144:147], v[206:209], v[92:95]
	v_mfma_f32_16x16x32_bf16 v[88:91], v[162:165], v[206:209], v[88:91]
	v_mfma_f32_16x16x32_bf16 v[76:79], v[144:147], v[214:217], v[76:79]
	v_mfma_f32_16x16x32_bf16 v[72:75], v[162:165], v[214:217], v[72:75]
	v_mfma_f32_16x16x32_bf16 v[124:127], v[158:161], v[190:193], v[124:127]
	v_mfma_f32_16x16x32_bf16 v[120:123], v[166:169], v[190:193], v[120:123]
	v_mfma_f32_16x16x32_bf16 v[108:111], v[158:161], v[202:205], v[108:111]
	v_mfma_f32_16x16x32_bf16 v[104:107], v[166:169], v[202:205], v[104:107]
	v_mfma_f32_16x16x32_bf16 v[92:95], v[158:161], v[210:213], v[92:95]
	v_mfma_f32_16x16x32_bf16 v[88:91], v[166:169], v[210:213], v[88:91]
	v_mfma_f32_16x16x32_bf16 v[76:79], v[158:161], v[218:221], v[76:79]
	v_mfma_f32_16x16x32_bf16 v[72:75], v[166:169], v[218:221], v[72:75]
	s_setprio 0
	s_setprio 1
	v_mfma_f32_16x16x32_bf16 v[116:119], v[170:173], v[186:189], v[116:119]
	v_mfma_f32_16x16x32_bf16 v[112:115], v[178:181], v[186:189], v[112:115]
	v_mfma_f32_16x16x32_bf16 v[100:103], v[170:173], v[194:197], v[100:103]
	v_mfma_f32_16x16x32_bf16 v[96:99], v[178:181], v[194:197], v[96:99]
	v_mfma_f32_16x16x32_bf16 v[84:87], v[170:173], v[206:209], v[84:87]
	v_mfma_f32_16x16x32_bf16 v[80:83], v[178:181], v[206:209], v[80:83]
	v_mfma_f32_16x16x32_bf16 v[68:71], v[170:173], v[214:217], v[68:71]
	v_mfma_f32_16x16x32_bf16 v[64:67], v[178:181], v[214:217], v[64:67]
	v_mfma_f32_16x16x32_bf16 v[116:119], v[174:177], v[190:193], v[116:119]
	v_mfma_f32_16x16x32_bf16 v[112:115], v[182:185], v[190:193], v[112:115]
	v_mfma_f32_16x16x32_bf16 v[100:103], v[174:177], v[202:205], v[100:103]
	v_mfma_f32_16x16x32_bf16 v[96:99], v[182:185], v[202:205], v[96:99]
	v_mfma_f32_16x16x32_bf16 v[84:87], v[174:177], v[210:213], v[84:87]
	v_mfma_f32_16x16x32_bf16 v[80:83], v[182:185], v[210:213], v[80:83]
	v_mfma_f32_16x16x32_bf16 v[68:71], v[174:177], v[218:221], v[68:71]
	v_mfma_f32_16x16x32_bf16 v[64:67], v[182:185], v[218:221], v[64:67]
	s_setprio 0
	s_barrier
	s_add_i32 s28, s52, s33
	v_lshl_add_u64 v[148:149], v[148:149], 0, s[18:19]
	s_mov_b32 m0, s28
	ds_read_b128 v[186:189], v155 offset:49152
	ds_read_b128 v[190:193], v155 offset:50176
	ds_read_b128 v[194:197], v155 offset:51200
	ds_read_b128 v[202:205], v155 offset:52224
	ds_read_b128 v[206:209], v155 offset:53248
	ds_read_b128 v[210:213], v155 offset:54272
	ds_read_b128 v[214:217], v155 offset:55296
	ds_read_b128 v[218:221], v155 offset:56320
	global_load_lds_dwordx4 v[148:149], off
	s_add_i32 m0, s28, 0x2000
	s_add_u32 s26, s26, 0xb0080
	v_lshl_add_u64 v[148:149], v[198:199], 0, s[18:19]
	s_addc_u32 s27, s27, 0
	s_add_i32 s28, s53, s33
	global_load_lds_dwordx4 v[148:149], off
	v_lshl_add_u64 v[148:149], s[26:27], 0, v[130:131]
	s_mov_b32 m0, s28
	s_nop 0
	global_load_lds_dwordx4 v[148:149], off
	v_lshl_add_u64 v[148:149], s[26:27], 0, v[134:135]
	s_add_i32 m0, s28, 0x2000
	s_nop 0
	global_load_lds_dwordx4 v[148:149], off
	v_lshl_add_u64 v[148:149], v[222:223], 0, s[18:19]
	s_mov_b32 m0, s39
	s_nop 0
	global_load_lds_dwordx4 v[148:149], off
	v_lshl_add_u64 v[148:149], v[224:225], 0, s[18:19]
	s_mov_b32 m0, s40
	s_nop 0
	global_load_lds_dwordx4 v[148:149], off
	s_waitcnt vmcnt(8)
	s_waitcnt lgkmcnt(0)
	s_barrier
	s_setprio 1
	s_waitcnt lgkmcnt(0)
	v_mfma_f32_16x16x32_bf16 v[60:63], v[144:147], v[186:189], v[60:63]
	v_mfma_f32_16x16x32_bf16 v[56:59], v[162:165], v[186:189], v[56:59]
	v_mfma_f32_16x16x32_bf16 v[44:47], v[144:147], v[194:197], v[44:47]
	v_mfma_f32_16x16x32_bf16 v[40:43], v[162:165], v[194:197], v[40:43]
	v_mfma_f32_16x16x32_bf16 v[28:31], v[144:147], v[206:209], v[28:31]
	v_mfma_f32_16x16x32_bf16 v[24:27], v[162:165], v[206:209], v[24:27]
	v_mfma_f32_16x16x32_bf16 v[12:15], v[144:147], v[214:217], v[12:15]
	v_mfma_f32_16x16x32_bf16 v[8:11], v[162:165], v[214:217], v[8:11]
	v_mfma_f32_16x16x32_bf16 v[60:63], v[158:161], v[190:193], v[60:63]
	v_mfma_f32_16x16x32_bf16 v[56:59], v[166:169], v[190:193], v[56:59]
	v_mfma_f32_16x16x32_bf16 v[44:47], v[158:161], v[202:205], v[44:47]
	v_mfma_f32_16x16x32_bf16 v[40:43], v[166:169], v[202:205], v[40:43]
	v_mfma_f32_16x16x32_bf16 v[28:31], v[158:161], v[210:213], v[28:31]
	v_mfma_f32_16x16x32_bf16 v[24:27], v[166:169], v[210:213], v[24:27]
	v_mfma_f32_16x16x32_bf16 v[12:15], v[158:161], v[218:221], v[12:15]
	v_mfma_f32_16x16x32_bf16 v[8:11], v[166:169], v[218:221], v[8:11]
	s_setprio 0
	s_setprio 1
	v_mfma_f32_16x16x32_bf16 v[52:55], v[170:173], v[186:189], v[52:55]
	v_mfma_f32_16x16x32_bf16 v[48:51], v[178:181], v[186:189], v[48:51]
	v_mfma_f32_16x16x32_bf16 v[36:39], v[170:173], v[194:197], v[36:39]
	v_mfma_f32_16x16x32_bf16 v[32:35], v[178:181], v[194:197], v[32:35]
	v_mfma_f32_16x16x32_bf16 v[20:23], v[170:173], v[206:209], v[20:23]
	v_mfma_f32_16x16x32_bf16 v[16:19], v[178:181], v[206:209], v[16:19]
	v_mfma_f32_16x16x32_bf16 v[4:7], v[170:173], v[214:217], v[4:7]
	v_mfma_f32_16x16x32_bf16 v[0:3], v[178:181], v[214:217], v[0:3]
	v_mfma_f32_16x16x32_bf16 v[52:55], v[174:177], v[190:193], v[52:55]
	v_mfma_f32_16x16x32_bf16 v[48:51], v[182:185], v[190:193], v[48:51]
	v_mfma_f32_16x16x32_bf16 v[36:39], v[174:177], v[202:205], v[36:39]
	v_mfma_f32_16x16x32_bf16 v[32:35], v[182:185], v[202:205], v[32:35]
	v_mfma_f32_16x16x32_bf16 v[20:23], v[174:177], v[210:213], v[20:23]
	v_mfma_f32_16x16x32_bf16 v[16:19], v[182:185], v[210:213], v[16:19]
	v_mfma_f32_16x16x32_bf16 v[4:7], v[174:177], v[218:221], v[4:7]
	v_mfma_f32_16x16x32_bf16 v[0:3], v[182:185], v[218:221], v[0:3]
	s_setprio 0
	s_add_i32 s51, s51, 2
	s_add_u32 s24, s24, 0x100
	s_addc_u32 s25, s25, 0
	s_add_u32 s0, s0, 0x100
	s_addc_u32 s50, s50, 0
	s_cmp_gt_u32 s51, 41
	s_barrier
	s_cbranch_scc0 .LBB0_1858
	s_and_b64 vcc, exec, s[20:21]
	s_cbranch_vccz .LBB0_1861
	s_barrier
